# load-early in all 24 K-loop load segments (adds the three phase-1 segments of the branch and expert-up loops by renaming the self-updated LDS address temporaries)
# baseline (speedup 1.0000x reference)
.LBB0_194:
	s_add_u32 s34, s92, 0xfffa0080
	s_addc_u32 s35, s93, -1
	s_add_i32 s2, 0, 0x10000
	s_cmp_eq_u32 s1, 12
	s_cselect_b32 s95, s57, s35
	s_cselect_b32 s94, vcc_lo, s34
	s_cselect_b32 s97, s55, s11
	s_cselect_b32 s96, vcc_hi, s10
	s_add_i32 s82, 0, 0x14000
	s_mov_b32 s34, 0xfffe0000
	s_mov_b32 s35, -1
	v_lshl_add_u64 v[168:169], s[92:93], 0, v[154:155]
	v_lshl_add_u64 v[168:169], v[168:169], 0, s[34:35]
	s_add_i32 m0, s89, 0xc000
	s_nop 0
	global_load_lds_dwordx4 v[168:169], off
	s_add_i32 m0, s89, 0xe000
	s_nop 0
	global_load_lds_dwordx4 v154, s[92:93]
	v_add_u32_e32 v146, s68, v174
	v_add_u32_e32 v142, s2, v146
	v_add_u32_e32 v164, s82, v146
	ds_read_b128 v[130:133], v142
	ds_read_b128 v[134:137], v142 offset:1024
	ds_read_b128 v[138:141], v142 offset:2048
	ds_read_b128 v[142:145], v142 offset:3072
	ds_read_b128 v[146:149], v164
	ds_read_b128 v[150:153], v164 offset:1024
	ds_read_b128 v[160:163], v164 offset:2048
	ds_read_b128 v[164:167], v164 offset:3072
	v_add_u32_e32 v159, s69, v174
	ds_read_b128 v[176:179], v159
	ds_read_b128 v[180:183], v159 offset:1024
	ds_read_b128 v[184:187], v159 offset:2048
	ds_read_b128 v[188:191], v159 offset:3072
	ds_read_b128 v[196:199], v159 offset:4096
	ds_read_b128 v[200:203], v159 offset:5120
	ds_read_b128 v[204:207], v159 offset:6144
	ds_read_b128 v[208:211], v159 offset:7168
	s_waitcnt vmcnt(8)
	s_waitcnt lgkmcnt(0)
	s_barrier
	s_setprio 1
	s_waitcnt lgkmcnt(0)
	v_mfma_scale_f32_16x16x128_f8f6f4 v[126:129], v[130:137], v[176:183], v[126:129], v1, v1 op_sel_hi:[0,0,0]
	v_mfma_scale_f32_16x16x128_f8f6f4 v[122:125], v[138:145], v[176:183], v[122:125], v1, v1 op_sel_hi:[0,0,0]
	v_mfma_scale_f32_16x16x128_f8f6f4 v[114:117], v[130:137], v[184:191], v[114:117], v1, v1 op_sel_hi:[0,0,0]
	v_mfma_scale_f32_16x16x128_f8f6f4 v[106:109], v[138:145], v[184:191], v[106:109], v1, v1 op_sel_hi:[0,0,0]
	v_mfma_scale_f32_16x16x128_f8f6f4 v[98:101], v[130:137], v[196:203], v[98:101], v1, v1 op_sel_hi:[0,0,0]
	v_mfma_scale_f32_16x16x128_f8f6f4 v[212:215], v[138:145], v[196:203], v[90:93], v1, v1 op_sel_hi:[0,0,0]
	v_mfma_scale_f32_16x16x128_f8f6f4 v[216:219], v[130:137], v[204:211], v[82:85], v1, v1 op_sel_hi:[0,0,0]
	v_mfma_scale_f32_16x16x128_f8f6f4 v[220:223], v[138:145], v[204:211], v[74:77], v1, v1 op_sel_hi:[0,0,0]
	s_setprio 0
	s_setprio 1
	v_mfma_scale_f32_16x16x128_f8f6f4 v[118:121], v[146:153], v[176:183], v[118:121], v1, v1 op_sel_hi:[0,0,0]
	v_mfma_scale_f32_16x16x128_f8f6f4 v[110:113], v[160:167], v[176:183], v[110:113], v1, v1 op_sel_hi:[0,0,0]
	v_mfma_scale_f32_16x16x128_f8f6f4 v[102:105], v[146:153], v[184:191], v[102:105], v1, v1 op_sel_hi:[0,0,0]
	v_mfma_scale_f32_16x16x128_f8f6f4 v[176:179], v[160:167], v[184:191], v[94:97], v1, v1 op_sel_hi:[0,0,0]
	v_mfma_scale_f32_16x16x128_f8f6f4 v[180:183], v[146:153], v[196:203], v[86:89], v1, v1 op_sel_hi:[0,0,0]
	v_mfma_scale_f32_16x16x128_f8f6f4 v[184:187], v[160:167], v[196:203], v[78:81], v1, v1 op_sel_hi:[0,0,0]
	v_mfma_scale_f32_16x16x128_f8f6f4 v[188:191], v[146:153], v[204:211], v[62:65], v1, v1 op_sel_hi:[0,0,0]
	v_mfma_scale_f32_16x16x128_f8f6f4 v[196:199], v[160:167], v[204:211], v[58:61], v1, v1 op_sel_hi:[0,0,0]
	s_setprio 0
	s_barrier
	v_mov_b32_e32 v159, v155
	v_add_u32_e32 v94, s69, v174
	s_add_i32 s2, s2, s6
	s_nop 1
	s_mov_b32 m0, s2
	v_lshl_add_u64 v[168:169], s[96:97], 0, v[158:159]
	global_load_lds_dwordx4 v158, s[96:97]
	v_lshl_add_u64 v[168:169], v[168:169], 0, s[14:15]
	s_add_i32 m0, s2, 0x2000
	s_add_i32 s2, s82, s6
	global_load_lds_dwordx4 v[168:169], off
	s_mov_b32 m0, s2
	v_lshl_add_u64 v[168:169], s[96:97], 0, v[158:159]
	v_lshl_add_u64 v[170:171], v[168:169], 0, s[16:17]
	global_load_lds_dwordx4 v[170:171], off
	v_lshl_add_u64 v[168:169], v[168:169], 0, s[18:19]
	s_add_i32 m0, s2, 0x2000
	s_nop 0
	global_load_lds_dwordx4 v[168:169], off
	s_mov_b32 m0, s89
	v_lshl_add_u64 v[168:169], s[94:95], 0, v[154:155]
	global_load_lds_dwordx4 v154, s[94:95]
	v_lshl_add_u64 v[168:169], v[168:169], 0, s[14:15]
	s_mov_b32 m0, s91
	s_nop 0
	global_load_lds_dwordx4 v[168:169], off
	ds_read_b128 v[58:61], v94 offset:16384
	ds_read_b128 v[62:65], v94 offset:17408
	ds_read_b128 v[74:77], v94 offset:18432
	ds_read_b128 v[78:81], v94 offset:19456
	ds_read_b128 v[82:85], v94 offset:20480
	ds_read_b128 v[86:89], v94 offset:21504
	ds_read_b128 v[90:93], v94 offset:22528
	ds_read_b128 v[94:97], v94 offset:23552
	s_waitcnt vmcnt(8)
	s_waitcnt lgkmcnt(0)
	s_barrier
	s_setprio 1
	s_waitcnt lgkmcnt(0)
	v_mfma_scale_f32_16x16x128_f8f6f4 v[54:57], v[130:137], v[58:65], v[54:57], v1, v1 op_sel_hi:[0,0,0]
	v_mfma_scale_f32_16x16x128_f8f6f4 v[200:203], v[138:145], v[58:65], v[42:45], v1, v1 op_sel_hi:[0,0,0]
	v_mfma_scale_f32_16x16x128_f8f6f4 v[204:207], v[130:137], v[74:81], v[30:33], v1, v1 op_sel_hi:[0,0,0]
	v_mfma_scale_f32_16x16x128_f8f6f4 v[208:211], v[138:145], v[74:81], v[26:29], v1, v1 op_sel_hi:[0,0,0]
	v_mfma_scale_f32_16x16x128_f8f6f4 v[224:227], v[130:137], v[82:89], v[14:17], v1, v1 op_sel_hi:[0,0,0]
	v_mfma_scale_f32_16x16x128_f8f6f4 v[228:231], v[138:145], v[82:89], v[10:13], v1, v1 op_sel_hi:[0,0,0]
	v_mfma_scale_f32_16x16x128_f8f6f4 v[232:235], v[130:137], v[90:97], v[6:9], v1, v1 op_sel_hi:[0,0,0]
	v_mfma_scale_f32_16x16x128_f8f6f4 v[236:239], v[138:145], v[90:97], v[2:5], v1, v1 op_sel_hi:[0,0,0]
	s_setprio 0
	s_setprio 1
	v_mfma_scale_f32_16x16x128_f8f6f4 v[66:69], v[146:153], v[58:65], v[66:69], v1, v1 op_sel_hi:[0,0,0]
	v_mfma_scale_f32_16x16x128_f8f6f4 v[70:73], v[160:167], v[58:65], v[70:73], v1, v1 op_sel_hi:[0,0,0]
	v_mfma_scale_f32_16x16x128_f8f6f4 v[50:53], v[160:167], v[74:81], v[50:53], v1, v1 op_sel_hi:[0,0,0]
	v_mfma_scale_f32_16x16x128_f8f6f4 v[240:243], v[146:153], v[74:81], v[46:49], v1, v1 op_sel_hi:[0,0,0]
	v_mfma_scale_f32_16x16x128_f8f6f4 v[244:247], v[146:153], v[82:89], v[34:37], v1, v1 op_sel_hi:[0,0,0]
	v_mfma_scale_f32_16x16x128_f8f6f4 v[248:251], v[160:167], v[82:89], v[38:41], v1, v1 op_sel_hi:[0,0,0]
	v_mfma_scale_f32_16x16x128_f8f6f4 v[192:195], v[146:153], v[90:97], v[18:21], v1, v1 op_sel_hi:[0,0,0]
	v_mfma_scale_f32_16x16x128_f8f6f4 v[168:171], v[160:167], v[90:97], v[22:25], v1, v1 op_sel_hi:[0,0,0]
	s_setprio 0
	s_barrier
	s_mov_b32 m0, s7
	v_lshl_add_u64 v[58:59], s[94:95], 0, v[154:155]
	v_lshl_add_u64 v[60:61], v[58:59], 0, s[16:17]
	global_load_lds_dwordx4 v[60:61], off
	v_lshl_add_u64 v[58:59], v[58:59], 0, s[18:19]
	s_mov_b32 m0, s0
	s_nop 0
	global_load_lds_dwordx4 v[58:59], off
	s_add_i32 s2, 0, 0x18000
	v_add_u32_e32 v10, s68, v174
	s_add_i32 s34, 0, 0x1c000
	v_add_u32_e32 v22, s2, v10
	v_add_u32_e32 v142, s34, v10
	ds_read_b128 v[2:5], v22
	ds_read_b128 v[6:9], v22 offset:1024
	ds_read_b128 v[18:21], v22 offset:2048
	ds_read_b128 v[22:25], v22 offset:3072
	ds_read_b128 v[130:133], v142
	ds_read_b128 v[134:137], v142 offset:1024
	ds_read_b128 v[138:141], v142 offset:2048
	ds_read_b128 v[142:145], v142 offset:3072
	v_add_u32_e32 v46, s69, v174
	ds_read_b128 v[10:13], v46 offset:32768
	ds_read_b128 v[14:17], v46 offset:33792
	ds_read_b128 v[26:29], v46 offset:34816
	ds_read_b128 v[30:33], v46 offset:35840
	ds_read_b128 v[34:37], v46 offset:36864
	ds_read_b128 v[38:41], v46 offset:37888
	ds_read_b128 v[42:45], v46 offset:38912
	ds_read_b128 v[46:49], v46 offset:39936
	s_waitcnt vmcnt(8)
	s_waitcnt lgkmcnt(0)
	s_barrier
	s_setprio 1
	s_waitcnt lgkmcnt(0)
	v_mfma_scale_f32_16x16x128_f8f6f4 v[126:129], v[2:9], v[10:17], v[126:129], v1, v1 op_sel_hi:[0,0,0]
	v_mfma_scale_f32_16x16x128_f8f6f4 v[122:125], v[18:25], v[10:17], v[122:125], v1, v1 op_sel_hi:[0,0,0]
	v_mfma_scale_f32_16x16x128_f8f6f4 v[114:117], v[2:9], v[26:33], v[114:117], v1, v1 op_sel_hi:[0,0,0]
	v_mfma_scale_f32_16x16x128_f8f6f4 v[106:109], v[18:25], v[26:33], v[106:109], v1, v1 op_sel_hi:[0,0,0]
	v_mfma_scale_f32_16x16x128_f8f6f4 v[98:101], v[2:9], v[34:41], v[98:101], v1, v1 op_sel_hi:[0,0,0]
	v_mfma_scale_f32_16x16x128_f8f6f4 v[90:93], v[18:25], v[34:41], v[212:215], v1, v1 op_sel_hi:[0,0,0]
	v_mfma_scale_f32_16x16x128_f8f6f4 v[82:85], v[2:9], v[42:49], v[216:219], v1, v1 op_sel_hi:[0,0,0]
	v_mfma_scale_f32_16x16x128_f8f6f4 v[74:77], v[18:25], v[42:49], v[220:223], v1, v1 op_sel_hi:[0,0,0]
	s_setprio 0
	s_setprio 1
	v_mfma_scale_f32_16x16x128_f8f6f4 v[118:121], v[130:137], v[10:17], v[118:121], v1, v1 op_sel_hi:[0,0,0]
	v_mfma_scale_f32_16x16x128_f8f6f4 v[110:113], v[138:145], v[10:17], v[110:113], v1, v1 op_sel_hi:[0,0,0]
	v_mfma_scale_f32_16x16x128_f8f6f4 v[102:105], v[130:137], v[26:33], v[102:105], v1, v1 op_sel_hi:[0,0,0]
	v_mfma_scale_f32_16x16x128_f8f6f4 v[94:97], v[138:145], v[26:33], v[176:179], v1, v1 op_sel_hi:[0,0,0]
	v_mfma_scale_f32_16x16x128_f8f6f4 v[86:89], v[130:137], v[34:41], v[180:183], v1, v1 op_sel_hi:[0,0,0]
	v_mfma_scale_f32_16x16x128_f8f6f4 v[78:81], v[138:145], v[34:41], v[184:187], v1, v1 op_sel_hi:[0,0,0]
	v_mfma_scale_f32_16x16x128_f8f6f4 v[62:65], v[130:137], v[42:49], v[188:191], v1, v1 op_sel_hi:[0,0,0]
	v_mfma_scale_f32_16x16x128_f8f6f4 v[58:61], v[138:145], v[42:49], v[196:199], v1, v1 op_sel_hi:[0,0,0]
	s_setprio 0
	s_barrier
	s_add_i32 s2, s2, s6
	s_mov_b32 m0, s2
	v_lshl_add_u64 v[10:11], s[96:97], 0, v[158:159]
	v_lshl_add_u64 v[12:13], v[10:11], 0, s[20:21]
	global_load_lds_dwordx4 v[12:13], off
	v_lshl_add_u64 v[10:11], v[10:11], 0, s[22:23]
	s_add_i32 m0, s2, 0x2000
	s_add_i32 s2, s34, s6
	global_load_lds_dwordx4 v[10:11], off
	s_mov_b32 m0, s2
	v_lshl_add_u64 v[10:11], s[96:97], 0, v[158:159]
	v_lshl_add_u64 v[12:13], v[10:11], 0, s[24:25]
	global_load_lds_dwordx4 v[12:13], off
	v_lshl_add_u64 v[10:11], v[10:11], 0, s[26:27]
	s_add_i32 m0, s2, 0x2000
	s_nop 0
	global_load_lds_dwordx4 v[10:11], off
	s_mov_b32 m0, s33
	v_lshl_add_u64 v[10:11], s[94:95], 0, v[154:155]
	v_lshl_add_u64 v[12:13], v[10:11], 0, s[20:21]
	global_load_lds_dwordx4 v[12:13], off
	v_lshl_add_u64 v[10:11], v[10:11], 0, s[22:23]
	s_mov_b32 m0, s76
	s_nop 0
	global_load_lds_dwordx4 v[10:11], off
	v_add_u32_e32 v180, s69, v174
	ds_read_b128 v[34:37], v180 offset:49152
	ds_read_b128 v[38:41], v180 offset:50176
	ds_read_b128 v[146:149], v180 offset:51200
	ds_read_b128 v[150:153], v180 offset:52224
	ds_read_b128 v[160:163], v180 offset:53248
	ds_read_b128 v[164:167], v180 offset:54272
	ds_read_b128 v[176:179], v180 offset:55296
	ds_read_b128 v[180:183], v180 offset:56320
	s_waitcnt vmcnt(8)
	s_waitcnt lgkmcnt(0)
	s_barrier
	s_setprio 1
	s_waitcnt lgkmcnt(0)
	v_mfma_scale_f32_16x16x128_f8f6f4 v[54:57], v[2:9], v[34:41], v[54:57], v1, v1 op_sel_hi:[0,0,0]
	v_mfma_scale_f32_16x16x128_f8f6f4 v[42:45], v[18:25], v[34:41], v[200:203], v1, v1 op_sel_hi:[0,0,0]
	v_mfma_scale_f32_16x16x128_f8f6f4 v[30:33], v[2:9], v[146:153], v[204:207], v1, v1 op_sel_hi:[0,0,0]
	v_mfma_scale_f32_16x16x128_f8f6f4 v[26:29], v[18:25], v[146:153], v[208:211], v1, v1 op_sel_hi:[0,0,0]
	v_mfma_scale_f32_16x16x128_f8f6f4 v[14:17], v[2:9], v[160:167], v[224:227], v1, v1 op_sel_hi:[0,0,0]
	v_mfma_scale_f32_16x16x128_f8f6f4 v[10:13], v[18:25], v[160:167], v[228:231], v1, v1 op_sel_hi:[0,0,0]
	v_mfma_scale_f32_16x16x128_f8f6f4 v[6:9], v[2:9], v[176:183], v[232:235], v1, v1 op_sel_hi:[0,0,0]
	v_mfma_scale_f32_16x16x128_f8f6f4 v[2:5], v[18:25], v[176:183], v[236:239], v1, v1 op_sel_hi:[0,0,0]
	s_setprio 0
	s_setprio 1
	v_mfma_scale_f32_16x16x128_f8f6f4 v[66:69], v[130:137], v[34:41], v[66:69], v1, v1 op_sel_hi:[0,0,0]
	v_mfma_scale_f32_16x16x128_f8f6f4 v[70:73], v[138:145], v[34:41], v[70:73], v1, v1 op_sel_hi:[0,0,0]
	v_mfma_scale_f32_16x16x128_f8f6f4 v[46:49], v[130:137], v[146:153], v[240:243], v1, v1 op_sel_hi:[0,0,0]
	v_mfma_scale_f32_16x16x128_f8f6f4 v[50:53], v[138:145], v[146:153], v[50:53], v1, v1 op_sel_hi:[0,0,0]
	v_mfma_scale_f32_16x16x128_f8f6f4 v[34:37], v[130:137], v[160:167], v[244:247], v1, v1 op_sel_hi:[0,0,0]
	v_mfma_scale_f32_16x16x128_f8f6f4 v[38:41], v[138:145], v[160:167], v[248:251], v1, v1 op_sel_hi:[0,0,0]
	v_mfma_scale_f32_16x16x128_f8f6f4 v[18:21], v[130:137], v[176:183], v[192:195], v1, v1 op_sel_hi:[0,0,0]
	v_mfma_scale_f32_16x16x128_f8f6f4 v[22:25], v[138:145], v[176:183], v[168:171], v1, v1 op_sel_hi:[0,0,0]
	s_setprio 0
	s_barrier
	s_add_i32 s1, s1, 2
	s_add_u32 s92, s92, 0x100
	s_addc_u32 s93, s93, 0
	s_add_u32 s10, s10, 0x100
	s_addc_u32 s11, s11, 0
	s_cmp_gt_u32 s1, 13
	s_cbranch_scc0 .LBB0_194
	s_and_b64 vcc, exec, s[64:65]
	s_cbranch_vccz .LBB0_197
	s_barrier

.LBB0_977:
	s_add_u32 s34, s58, 0xfffd0080
	v_add_u32_e32 v46, s84, v1
	v_add_u32_e32 v142, s88, v46
	v_add_u32_e32 v158, s89, v46
	s_addc_u32 s35, s59, -1
	s_cmp_eq_u32 s70, 4
	s_cselect_b32 s61, s38, s35
	s_cselect_b32 s60, s39, s34
	s_cselect_b32 s63, s45, s69
	s_cselect_b32 s62, s47, s68
	s_mov_b32 s34, 0xffff0000
	s_mov_b32 s35, -1
	v_lshl_add_u64 v[46:47], s[58:59], 0, v[196:197]
	v_lshl_add_u64 v[46:47], v[46:47], 0, s[34:35]
	s_add_i32 m0, s64, 0xc000
	s_nop 0
	global_load_lds_dwordx4 v[46:47], off
	s_add_i32 m0, s64, 0xe000
	s_nop 0
	global_load_lds_dwordx4 v196, s[58:59]
	ds_read_b128 v[130:133], v142
	ds_read_b128 v[134:137], v142 offset:1024
	ds_read_b128 v[138:141], v142 offset:2048
	ds_read_b128 v[142:145], v142 offset:3072
	ds_read_b128 v[146:149], v158
	ds_read_b128 v[150:153], v158 offset:1024
	ds_read_b128 v[154:157], v158 offset:2048
	ds_read_b128 v[158:161], v158 offset:3072
	v_add_u32_e32 v190, s85, v1
	ds_read_b128 v[162:165], v190
	ds_read_b128 v[166:169], v190 offset:1024
	ds_read_b128 v[170:173], v190 offset:2048
	ds_read_b128 v[174:177], v190 offset:3072
	ds_read_b128 v[178:181], v190 offset:4096
	ds_read_b128 v[182:185], v190 offset:5120
	ds_read_b128 v[186:189], v190 offset:6144
	ds_read_b128 v[190:193], v190 offset:7168
	s_waitcnt vmcnt(8)
	s_waitcnt lgkmcnt(0)
	s_barrier
	s_setprio 1
	s_waitcnt lgkmcnt(0)
	v_mfma_scale_f32_16x16x128_f8f6f4 v[94:97], v[130:137], v[162:169], v[94:97], v195, v195 op_sel_hi:[0,0,0]
	v_mfma_scale_f32_16x16x128_f8f6f4 v[90:93], v[138:145], v[162:169], v[90:93], v195, v195 op_sel_hi:[0,0,0]
	v_mfma_scale_f32_16x16x128_f8f6f4 v[86:89], v[130:137], v[170:177], v[86:89], v195, v195 op_sel_hi:[0,0,0]
	v_mfma_scale_f32_16x16x128_f8f6f4 v[82:85], v[138:145], v[170:177], v[82:85], v195, v195 op_sel_hi:[0,0,0]
	v_mfma_scale_f32_16x16x128_f8f6f4 v[78:81], v[130:137], v[178:185], v[78:81], v195, v195 op_sel_hi:[0,0,0]
	v_mfma_scale_f32_16x16x128_f8f6f4 v[204:207], v[138:145], v[178:185], v[74:77], v195, v195 op_sel_hi:[0,0,0]
	v_mfma_scale_f32_16x16x128_f8f6f4 v[208:211], v[130:137], v[186:193], v[70:73], v195, v195 op_sel_hi:[0,0,0]
	v_mfma_scale_f32_16x16x128_f8f6f4 v[212:215], v[138:145], v[186:193], v[66:69], v195, v195 op_sel_hi:[0,0,0]
	s_setprio 0
	s_setprio 1
	v_mfma_scale_f32_16x16x128_f8f6f4 v[38:41], v[154:161], v[178:185], v[38:41], v195, v195 op_sel_hi:[0,0,0]
	v_mfma_scale_f32_16x16x128_f8f6f4 v[216:219], v[146:153], v[162:169], v[62:65], v195, v195 op_sel_hi:[0,0,0]
	v_mfma_scale_f32_16x16x128_f8f6f4 v[162:165], v[154:161], v[162:169], v[58:61], v195, v195 op_sel_hi:[0,0,0]
	v_mfma_scale_f32_16x16x128_f8f6f4 v[166:169], v[146:153], v[170:177], v[54:57], v195, v195 op_sel_hi:[0,0,0]
	v_mfma_scale_f32_16x16x128_f8f6f4 v[170:173], v[154:161], v[170:177], v[14:17], v195, v195 op_sel_hi:[0,0,0]
	v_mfma_scale_f32_16x16x128_f8f6f4 v[174:177], v[146:153], v[178:185], v[10:13], v195, v195 op_sel_hi:[0,0,0]
	v_mfma_scale_f32_16x16x128_f8f6f4 v[178:181], v[146:153], v[186:193], v[30:33], v195, v195 op_sel_hi:[0,0,0]
	v_mfma_scale_f32_16x16x128_f8f6f4 v[182:185], v[154:161], v[186:193], v[22:25], v195, v195 op_sel_hi:[0,0,0]
	s_setprio 0
	s_barrier
	v_mov_b32_e32 v203, v197
	s_nop 1
	s_add_i32 s34, s88, s43
	s_mov_b32 m0, s34
	v_lshl_add_u64 v[10:11], s[62:63], 0, v[202:203]
	global_load_lds_dwordx4 v202, s[62:63]
	v_lshl_add_u64 v[10:11], v[10:11], 0, s[12:13]
	s_add_i32 m0, s34, 0x2000
	s_add_i32 s34, s89, s43
	global_load_lds_dwordx4 v[10:11], off
	s_mov_b32 m0, s34
	v_lshl_add_u64 v[10:11], s[62:63], 0, v[202:203]
	v_lshl_add_u64 v[12:13], v[10:11], 0, s[14:15]
	global_load_lds_dwordx4 v[12:13], off
	v_lshl_add_u64 v[10:11], v[10:11], 0, s[16:17]
	s_add_i32 m0, s34, 0x2000
	s_nop 0
	global_load_lds_dwordx4 v[10:11], off
	s_mov_b32 m0, s64
	v_lshl_add_u64 v[10:11], s[60:61], 0, v[196:197]
	global_load_lds_dwordx4 v196, s[60:61]
	v_lshl_add_u64 v[10:11], v[10:11], 0, s[12:13]
	s_mov_b32 m0, s65
	s_nop 0
	global_load_lds_dwordx4 v[10:11], off
	v_add_u32_e32 v74, s85, v1
	ds_read_b128 v[46:49], v74 offset:16384
	ds_read_b128 v[50:53], v74 offset:17408
	ds_read_b128 v[54:57], v74 offset:18432
	ds_read_b128 v[58:61], v74 offset:19456
	ds_read_b128 v[62:65], v74 offset:20480
	ds_read_b128 v[66:69], v74 offset:21504
	ds_read_b128 v[70:73], v74 offset:22528
	ds_read_b128 v[74:77], v74 offset:23552
	s_waitcnt vmcnt(8)
	s_waitcnt lgkmcnt(0)
	s_barrier
	s_setprio 1
	s_waitcnt lgkmcnt(0)
	v_mfma_scale_f32_16x16x128_f8f6f4 v[42:45], v[130:137], v[46:53], v[42:45], v195, v195 op_sel_hi:[0,0,0]
	v_mfma_scale_f32_16x16x128_f8f6f4 v[34:37], v[138:145], v[46:53], v[34:37], v195, v195 op_sel_hi:[0,0,0]
	v_mfma_scale_f32_16x16x128_f8f6f4 v[224:227], v[130:137], v[62:69], v[224:227], v195, v195 op_sel_hi:[0,0,0]
	v_mfma_scale_f32_16x16x128_f8f6f4 v[228:231], v[138:145], v[62:69], v[228:231], v195, v195 op_sel_hi:[0,0,0]
	v_mfma_scale_f32_16x16x128_f8f6f4 v[186:189], v[130:137], v[54:61], v[26:29], v195, v195 op_sel_hi:[0,0,0]
	v_mfma_scale_f32_16x16x128_f8f6f4 v[190:193], v[138:145], v[54:61], v[18:21], v195, v195 op_sel_hi:[0,0,0]
	v_mfma_scale_f32_16x16x128_f8f6f4 v[232:235], v[130:137], v[70:77], v[6:9], v195, v195 op_sel_hi:[0,0,0]
	v_mfma_scale_f32_16x16x128_f8f6f4 v[236:239], v[138:145], v[70:77], v[2:5], v195, v195 op_sel_hi:[0,0,0]
	s_setprio 0
	s_setprio 1
	v_mfma_scale_f32_16x16x128_f8f6f4 v[240:243], v[146:153], v[46:53], v[98:101], v195, v195 op_sel_hi:[0,0,0]
	v_mfma_scale_f32_16x16x128_f8f6f4 v[244:247], v[154:161], v[46:53], v[102:105], v195, v195 op_sel_hi:[0,0,0]
	v_mfma_scale_f32_16x16x128_f8f6f4 v[248:251], v[146:153], v[54:61], v[106:109], v195, v195 op_sel_hi:[0,0,0]
	v_mfma_scale_f32_16x16x128_f8f6f4 v[198:201], v[154:161], v[54:61], v[110:113], v195, v195 op_sel_hi:[0,0,0]
	v_mfma_scale_f32_16x16x128_f8f6f4 v[220:223], v[146:153], v[62:69], v[114:117], v195, v195 op_sel_hi:[0,0,0]
	v_mfma_scale_f32_16x16x128_f8f6f4 v[46:49], v[154:161], v[62:69], v[118:121], v195, v195 op_sel_hi:[0,0,0]
	v_mfma_scale_f32_16x16x128_f8f6f4 v[50:53], v[146:153], v[70:77], v[122:125], v195, v195 op_sel_hi:[0,0,0]
	v_mfma_scale_f32_16x16x128_f8f6f4 v[154:157], v[154:161], v[70:77], v[126:129], v195, v195 op_sel_hi:[0,0,0]
	s_setprio 0
	s_barrier
	s_mov_b32 m0, s66
	v_lshl_add_u64 v[54:55], s[60:61], 0, v[196:197]
	v_lshl_add_u64 v[56:57], v[54:55], 0, s[14:15]
	global_load_lds_dwordx4 v[56:57], off
	v_lshl_add_u64 v[54:55], v[54:55], 0, s[16:17]
	s_mov_b32 m0, s67
	s_nop 0
	global_load_lds_dwordx4 v[54:55], off
	s_add_i32 s34, 0, 0x18000
	v_add_u32_e32 v10, s84, v1
	s_add_i32 s35, 0, 0x1c000
	v_add_u32_e32 v102, s34, v10
	v_add_u32_e32 v134, s35, v10
	ds_read_b128 v[2:5], v102
	ds_read_b128 v[6:9], v102 offset:1024
	ds_read_b128 v[98:101], v102 offset:2048
	ds_read_b128 v[102:105], v102 offset:3072
	ds_read_b128 v[122:125], v134
	ds_read_b128 v[126:129], v134 offset:1024
	ds_read_b128 v[130:133], v134 offset:2048
	ds_read_b128 v[134:137], v134 offset:3072
	v_add_u32_e32 v110, s85, v1
	ds_read_b128 v[10:13], v110 offset:32768
	ds_read_b128 v[14:17], v110 offset:33792
	ds_read_b128 v[18:21], v110 offset:34816
	ds_read_b128 v[22:25], v110 offset:35840
	ds_read_b128 v[26:29], v110 offset:36864
	ds_read_b128 v[30:33], v110 offset:37888
	ds_read_b128 v[106:109], v110 offset:38912
	ds_read_b128 v[110:113], v110 offset:39936
	s_waitcnt vmcnt(8)
	s_waitcnt lgkmcnt(0)
	s_barrier
	s_setprio 1
	s_waitcnt lgkmcnt(0)
	v_mfma_scale_f32_16x16x128_f8f6f4 v[94:97], v[2:9], v[10:17], v[94:97], v195, v195 op_sel_hi:[0,0,0]
	v_mfma_scale_f32_16x16x128_f8f6f4 v[90:93], v[98:105], v[10:17], v[90:93], v195, v195 op_sel_hi:[0,0,0]
	v_mfma_scale_f32_16x16x128_f8f6f4 v[86:89], v[2:9], v[18:25], v[86:89], v195, v195 op_sel_hi:[0,0,0]
	v_mfma_scale_f32_16x16x128_f8f6f4 v[82:85], v[98:105], v[18:25], v[82:85], v195, v195 op_sel_hi:[0,0,0]
	v_mfma_scale_f32_16x16x128_f8f6f4 v[78:81], v[2:9], v[26:33], v[78:81], v195, v195 op_sel_hi:[0,0,0]
	v_mfma_scale_f32_16x16x128_f8f6f4 v[74:77], v[98:105], v[26:33], v[204:207], v195, v195 op_sel_hi:[0,0,0]
	v_mfma_scale_f32_16x16x128_f8f6f4 v[70:73], v[2:9], v[106:113], v[208:211], v195, v195 op_sel_hi:[0,0,0]
	v_mfma_scale_f32_16x16x128_f8f6f4 v[66:69], v[98:105], v[106:113], v[212:215], v195, v195 op_sel_hi:[0,0,0]
	s_setprio 0
	s_setprio 1
	v_mfma_scale_f32_16x16x128_f8f6f4 v[62:65], v[122:129], v[10:17], v[216:219], v195, v195 op_sel_hi:[0,0,0]
	v_mfma_scale_f32_16x16x128_f8f6f4 v[58:61], v[130:137], v[10:17], v[162:165], v195, v195 op_sel_hi:[0,0,0]
	v_mfma_scale_f32_16x16x128_f8f6f4 v[54:57], v[122:129], v[18:25], v[166:169], v195, v195 op_sel_hi:[0,0,0]
	v_mfma_scale_f32_16x16x128_f8f6f4 v[14:17], v[130:137], v[18:25], v[170:173], v195, v195 op_sel_hi:[0,0,0]
	v_mfma_scale_f32_16x16x128_f8f6f4 v[10:13], v[122:129], v[26:33], v[174:177], v195, v195 op_sel_hi:[0,0,0]
	v_mfma_scale_f32_16x16x128_f8f6f4 v[38:41], v[130:137], v[26:33], v[38:41], v195, v195 op_sel_hi:[0,0,0]
	v_mfma_scale_f32_16x16x128_f8f6f4 v[30:33], v[122:129], v[106:113], v[178:181], v195, v195 op_sel_hi:[0,0,0]
	v_mfma_scale_f32_16x16x128_f8f6f4 v[22:25], v[130:137], v[106:113], v[182:185], v195, v195 op_sel_hi:[0,0,0]
	s_setprio 0
	s_barrier
	s_add_i32 s34, s34, s43
	s_mov_b32 m0, s34
	v_lshl_add_u64 v[18:19], s[62:63], 0, v[202:203]
	v_lshl_add_u64 v[20:21], v[18:19], 0, s[24:25]
	global_load_lds_dwordx4 v[20:21], off
	v_lshl_add_u64 v[18:19], v[18:19], 0, s[26:27]
	s_add_i32 m0, s34, 0x2000
	s_add_i32 s34, s35, s43
	global_load_lds_dwordx4 v[18:19], off
	s_mov_b32 m0, s34
	v_lshl_add_u64 v[18:19], s[62:63], 0, v[202:203]
	v_lshl_add_u64 v[20:21], v[18:19], 0, s[28:29]
	global_load_lds_dwordx4 v[20:21], off
	v_lshl_add_u64 v[18:19], v[18:19], 0, s[30:31]
	s_add_i32 m0, s34, 0x2000
	s_nop 0
	global_load_lds_dwordx4 v[18:19], off
	s_mov_b32 m0, s82
	v_lshl_add_u64 v[18:19], s[60:61], 0, v[196:197]
	v_lshl_add_u64 v[20:21], v[18:19], 0, s[24:25]
	global_load_lds_dwordx4 v[20:21], off
	v_lshl_add_u64 v[18:19], v[18:19], 0, s[26:27]
	s_mov_b32 m0, s83
	s_nop 0
	global_load_lds_dwordx4 v[18:19], off
	v_add_u32_e32 v150, s85, v1
	ds_read_b128 v[106:109], v150 offset:49152
	ds_read_b128 v[110:113], v150 offset:50176
	ds_read_b128 v[114:117], v150 offset:51200
	ds_read_b128 v[118:121], v150 offset:52224
	ds_read_b128 v[138:141], v150 offset:53248
	ds_read_b128 v[142:145], v150 offset:54272
	ds_read_b128 v[146:149], v150 offset:55296
	ds_read_b128 v[150:153], v150 offset:56320
	s_waitcnt vmcnt(8)
	s_waitcnt lgkmcnt(0)
	s_barrier
	s_setprio 1
	s_waitcnt lgkmcnt(0)
	v_mfma_scale_f32_16x16x128_f8f6f4 v[42:45], v[2:9], v[106:113], v[42:45], v195, v195 op_sel_hi:[0,0,0]
	v_mfma_scale_f32_16x16x128_f8f6f4 v[34:37], v[98:105], v[106:113], v[34:37], v195, v195 op_sel_hi:[0,0,0]
	v_mfma_scale_f32_16x16x128_f8f6f4 v[26:29], v[2:9], v[114:121], v[186:189], v195, v195 op_sel_hi:[0,0,0]
	v_mfma_scale_f32_16x16x128_f8f6f4 v[18:21], v[98:105], v[114:121], v[190:193], v195, v195 op_sel_hi:[0,0,0]
	v_mfma_scale_f32_16x16x128_f8f6f4 v[224:227], v[2:9], v[138:145], v[224:227], v195, v195 op_sel_hi:[0,0,0]
	v_mfma_scale_f32_16x16x128_f8f6f4 v[228:231], v[98:105], v[138:145], v[228:231], v195, v195 op_sel_hi:[0,0,0]
	v_mfma_scale_f32_16x16x128_f8f6f4 v[6:9], v[2:9], v[146:153], v[232:235], v195, v195 op_sel_hi:[0,0,0]
	v_mfma_scale_f32_16x16x128_f8f6f4 v[2:5], v[98:105], v[146:153], v[236:239], v195, v195 op_sel_hi:[0,0,0]
	s_setprio 0
	s_setprio 1
	v_mfma_scale_f32_16x16x128_f8f6f4 v[98:101], v[122:129], v[106:113], v[240:243], v195, v195 op_sel_hi:[0,0,0]
	v_mfma_scale_f32_16x16x128_f8f6f4 v[102:105], v[130:137], v[106:113], v[244:247], v195, v195 op_sel_hi:[0,0,0]
	v_mfma_scale_f32_16x16x128_f8f6f4 v[106:109], v[122:129], v[114:121], v[248:251], v195, v195 op_sel_hi:[0,0,0]
	v_mfma_scale_f32_16x16x128_f8f6f4 v[110:113], v[130:137], v[114:121], v[198:201], v195, v195 op_sel_hi:[0,0,0]
	v_mfma_scale_f32_16x16x128_f8f6f4 v[114:117], v[122:129], v[138:145], v[220:223], v195, v195 op_sel_hi:[0,0,0]
	v_mfma_scale_f32_16x16x128_f8f6f4 v[118:121], v[130:137], v[138:145], v[46:49], v195, v195 op_sel_hi:[0,0,0]
	v_mfma_scale_f32_16x16x128_f8f6f4 v[122:125], v[122:129], v[146:153], v[50:53], v195, v195 op_sel_hi:[0,0,0]
	v_mfma_scale_f32_16x16x128_f8f6f4 v[126:129], v[130:137], v[146:153], v[154:157], v195, v195 op_sel_hi:[0,0,0]
	s_setprio 0
	s_barrier
	s_add_i32 s70, s70, 2
	s_add_u32 s58, s58, 0x100
	s_addc_u32 s59, s59, 0
	s_add_u32 s68, s68, 0x100
	s_addc_u32 s69, s69, 0
	s_cmp_gt_u32 s70, 5
	s_cbranch_scc0 .LBB0_977
	s_and_b64 vcc, exec, s[36:37]
	s_cbranch_vccz .LBB0_980
	s_barrier

.LBB0_1074:
	s_add_u32 s2, s54, 0xfffa0080
	s_addc_u32 s34, s55, -1
	s_cmp_eq_u32 s76, 12
	s_cselect_b32 s57, s38, s34
	s_cselect_b32 s56, s39, s2
	s_cselect_b32 s59, s41, s75
	s_cselect_b32 s58, s43, s74
	s_mov_b32 s34, 0xfffe0000
	s_mov_b32 s35, -1
	v_lshl_add_u64 v[154:155], s[54:55], 0, v[158:159]
	v_lshl_add_u64 v[154:155], v[154:155], 0, s[34:35]
	s_add_i32 m0, s51, 0xc000
	s_nop 0
	global_load_lds_dwordx4 v[154:155], off
	s_add_i32 m0, s51, 0xe000
	s_nop 0
	global_load_lds_dwordx4 v158, s[54:55]
	v_add_u32_e32 v146, s66, v1
	v_add_u32_e32 v142, s71, v146
	v_add_u32_e32 v176, s72, v146
	ds_read_b128 v[130:133], v142
	ds_read_b128 v[134:137], v142 offset:1024
	ds_read_b128 v[138:141], v142 offset:2048
	ds_read_b128 v[142:145], v142 offset:3072
	ds_read_b128 v[146:149], v176
	ds_read_b128 v[150:153], v176 offset:1024
	ds_read_b128 v[172:175], v176 offset:2048
	ds_read_b128 v[176:179], v176 offset:3072
	v_add_u32_e32 v216, s67, v1
	ds_read_b128 v[180:183], v216
	ds_read_b128 v[184:187], v216 offset:1024
	ds_read_b128 v[196:199], v216 offset:2048
	ds_read_b128 v[200:203], v216 offset:3072
	ds_read_b128 v[204:207], v216 offset:4096
	ds_read_b128 v[208:211], v216 offset:5120
	ds_read_b128 v[212:215], v216 offset:6144
	ds_read_b128 v[216:219], v216 offset:7168
	s_waitcnt vmcnt(8)
	s_waitcnt lgkmcnt(0)
	s_barrier
	s_setprio 1
	s_waitcnt lgkmcnt(0)
	v_mfma_scale_f32_16x16x128_f8f6f4 v[126:129], v[130:137], v[180:187], v[126:129], v170, v170 op_sel_hi:[0,0,0]
	v_mfma_scale_f32_16x16x128_f8f6f4 v[122:125], v[138:145], v[180:187], v[122:125], v170, v170 op_sel_hi:[0,0,0]
	v_mfma_scale_f32_16x16x128_f8f6f4 v[114:117], v[130:137], v[196:203], v[114:117], v170, v170 op_sel_hi:[0,0,0]
	v_mfma_scale_f32_16x16x128_f8f6f4 v[106:109], v[138:145], v[196:203], v[106:109], v170, v170 op_sel_hi:[0,0,0]
	v_mfma_scale_f32_16x16x128_f8f6f4 v[98:101], v[130:137], v[204:211], v[98:101], v170, v170 op_sel_hi:[0,0,0]
	v_mfma_scale_f32_16x16x128_f8f6f4 v[154:157], v[138:145], v[204:211], v[90:93], v170, v170 op_sel_hi:[0,0,0]
	v_mfma_scale_f32_16x16x128_f8f6f4 v[166:169], v[130:137], v[212:219], v[82:85], v170, v170 op_sel_hi:[0,0,0]
	v_mfma_scale_f32_16x16x128_f8f6f4 v[188:191], v[138:145], v[212:219], v[74:77], v170, v170 op_sel_hi:[0,0,0]
	s_setprio 0
	s_setprio 1
	v_mfma_scale_f32_16x16x128_f8f6f4 v[118:121], v[146:153], v[180:187], v[118:121], v170, v170 op_sel_hi:[0,0,0]
	v_mfma_scale_f32_16x16x128_f8f6f4 v[110:113], v[172:179], v[180:187], v[110:113], v170, v170 op_sel_hi:[0,0,0]
	v_mfma_scale_f32_16x16x128_f8f6f4 v[102:105], v[146:153], v[196:203], v[102:105], v170, v170 op_sel_hi:[0,0,0]
	v_mfma_scale_f32_16x16x128_f8f6f4 v[180:183], v[172:179], v[196:203], v[94:97], v170, v170 op_sel_hi:[0,0,0]
	v_mfma_scale_f32_16x16x128_f8f6f4 v[184:187], v[146:153], v[204:211], v[86:89], v170, v170 op_sel_hi:[0,0,0]
	v_mfma_scale_f32_16x16x128_f8f6f4 v[192:195], v[172:179], v[204:211], v[78:81], v170, v170 op_sel_hi:[0,0,0]
	v_mfma_scale_f32_16x16x128_f8f6f4 v[196:199], v[146:153], v[212:219], v[70:73], v170, v170 op_sel_hi:[0,0,0]
	v_mfma_scale_f32_16x16x128_f8f6f4 v[200:203], v[172:179], v[212:219], v[66:69], v170, v170 op_sel_hi:[0,0,0]
	s_setprio 0
	s_barrier
	v_mov_b32_e32 v165, v159
	v_add_u32_e32 v94, s67, v1
	s_add_i32 s2, s71, s37
	s_nop 1
	s_mov_b32 m0, s2
	v_lshl_add_u64 v[204:205], s[58:59], 0, v[164:165]
	global_load_lds_dwordx4 v164, s[58:59]
	v_lshl_add_u64 v[204:205], v[204:205], 0, s[12:13]
	s_add_i32 m0, s2, 0x2000
	s_add_i32 s2, s72, s37
	global_load_lds_dwordx4 v[204:205], off
	s_mov_b32 m0, s2
	v_lshl_add_u64 v[204:205], s[58:59], 0, v[164:165]
	v_lshl_add_u64 v[206:207], v[204:205], 0, s[14:15]
	global_load_lds_dwordx4 v[206:207], off
	v_lshl_add_u64 v[204:205], v[204:205], 0, s[16:17]
	s_add_i32 m0, s2, 0x2000
	s_nop 0
	global_load_lds_dwordx4 v[204:205], off
	s_mov_b32 m0, s51
	v_lshl_add_u64 v[204:205], s[56:57], 0, v[158:159]
	global_load_lds_dwordx4 v158, s[56:57]
	v_lshl_add_u64 v[204:205], v[204:205], 0, s[12:13]
	s_mov_b32 m0, s60
	s_nop 0
	global_load_lds_dwordx4 v[204:205], off
	ds_read_b128 v[66:69], v94 offset:16384
	ds_read_b128 v[70:73], v94 offset:17408
	ds_read_b128 v[74:77], v94 offset:18432
	ds_read_b128 v[78:81], v94 offset:19456
	ds_read_b128 v[82:85], v94 offset:20480
	ds_read_b128 v[86:89], v94 offset:21504
	ds_read_b128 v[90:93], v94 offset:22528
	ds_read_b128 v[94:97], v94 offset:23552
	s_waitcnt vmcnt(8)
	s_waitcnt lgkmcnt(0)
	s_barrier
	s_setprio 1
	s_waitcnt lgkmcnt(0)
	v_mfma_scale_f32_16x16x128_f8f6f4 v[54:57], v[130:137], v[66:73], v[54:57], v170, v170 op_sel_hi:[0,0,0]
	v_mfma_scale_f32_16x16x128_f8f6f4 v[18:21], v[130:137], v[82:89], v[18:21], v170, v170 op_sel_hi:[0,0,0]
	v_mfma_scale_f32_16x16x128_f8f6f4 v[204:207], v[138:145], v[66:73], v[50:53], v170, v170 op_sel_hi:[0,0,0]
	v_mfma_scale_f32_16x16x128_f8f6f4 v[208:211], v[130:137], v[74:81], v[38:41], v170, v170 op_sel_hi:[0,0,0]
	v_mfma_scale_f32_16x16x128_f8f6f4 v[212:215], v[138:145], v[74:81], v[30:33], v170, v170 op_sel_hi:[0,0,0]
	v_mfma_scale_f32_16x16x128_f8f6f4 v[216:219], v[138:145], v[82:89], v[10:13], v170, v170 op_sel_hi:[0,0,0]
	v_mfma_scale_f32_16x16x128_f8f6f4 v[220:223], v[130:137], v[90:97], v[6:9], v170, v170 op_sel_hi:[0,0,0]
	v_mfma_scale_f32_16x16x128_f8f6f4 v[224:227], v[138:145], v[90:97], v[2:5], v170, v170 op_sel_hi:[0,0,0]
	s_setprio 0
	s_setprio 1
	v_mfma_scale_f32_16x16x128_f8f6f4 v[62:65], v[146:153], v[66:73], v[62:65], v170, v170 op_sel_hi:[0,0,0]
	v_mfma_scale_f32_16x16x128_f8f6f4 v[58:61], v[172:179], v[66:73], v[58:61], v170, v170 op_sel_hi:[0,0,0]
	v_mfma_scale_f32_16x16x128_f8f6f4 v[228:231], v[146:153], v[74:81], v[46:49], v170, v170 op_sel_hi:[0,0,0]
	v_mfma_scale_f32_16x16x128_f8f6f4 v[232:235], v[172:179], v[74:81], v[42:45], v170, v170 op_sel_hi:[0,0,0]
	v_mfma_scale_f32_16x16x128_f8f6f4 v[236:239], v[146:153], v[82:89], v[34:37], v170, v170 op_sel_hi:[0,0,0]
	v_mfma_scale_f32_16x16x128_f8f6f4 v[240:243], v[172:179], v[82:89], v[26:29], v170, v170 op_sel_hi:[0,0,0]
	v_mfma_scale_f32_16x16x128_f8f6f4 v[244:247], v[146:153], v[90:97], v[22:25], v170, v170 op_sel_hi:[0,0,0]
	v_mfma_scale_f32_16x16x128_f8f6f4 v[248:251], v[172:179], v[90:97], v[14:17], v170, v170 op_sel_hi:[0,0,0]
	s_setprio 0
	s_barrier
	s_mov_b32 m0, s61
	v_lshl_add_u64 v[66:67], s[56:57], 0, v[158:159]
	v_lshl_add_u64 v[68:69], v[66:67], 0, s[14:15]
	global_load_lds_dwordx4 v[68:69], off
	v_lshl_add_u64 v[66:67], v[66:67], 0, s[16:17]
	s_mov_b32 m0, s62
	s_nop 0
	global_load_lds_dwordx4 v[66:67], off
	s_add_i32 s2, 0, 0x18000
	v_add_u32_e32 v10, s66, v1
	s_add_i32 s34, 0, 0x1c000
	v_add_u32_e32 v26, s2, v10
	v_add_u32_e32 v142, s34, v10
	ds_read_b128 v[2:5], v26
	ds_read_b128 v[6:9], v26 offset:1024
	ds_read_b128 v[22:25], v26 offset:2048
	ds_read_b128 v[26:29], v26 offset:3072
	ds_read_b128 v[130:133], v142
	ds_read_b128 v[134:137], v142 offset:1024
	ds_read_b128 v[138:141], v142 offset:2048
	ds_read_b128 v[142:145], v142 offset:3072
	v_add_u32_e32 v50, s67, v1
	ds_read_b128 v[10:13], v50 offset:32768
	ds_read_b128 v[14:17], v50 offset:33792
	ds_read_b128 v[30:33], v50 offset:34816
	ds_read_b128 v[34:37], v50 offset:35840
	ds_read_b128 v[38:41], v50 offset:36864
	ds_read_b128 v[42:45], v50 offset:37888
	ds_read_b128 v[46:49], v50 offset:38912
	ds_read_b128 v[50:53], v50 offset:39936
	s_waitcnt vmcnt(8)
	s_waitcnt lgkmcnt(0)
	s_barrier
	s_setprio 1
	s_waitcnt lgkmcnt(0)
	v_mfma_scale_f32_16x16x128_f8f6f4 v[126:129], v[2:9], v[10:17], v[126:129], v170, v170 op_sel_hi:[0,0,0]
	v_mfma_scale_f32_16x16x128_f8f6f4 v[122:125], v[22:29], v[10:17], v[122:125], v170, v170 op_sel_hi:[0,0,0]
	v_mfma_scale_f32_16x16x128_f8f6f4 v[114:117], v[2:9], v[30:37], v[114:117], v170, v170 op_sel_hi:[0,0,0]
	v_mfma_scale_f32_16x16x128_f8f6f4 v[106:109], v[22:29], v[30:37], v[106:109], v170, v170 op_sel_hi:[0,0,0]
	v_mfma_scale_f32_16x16x128_f8f6f4 v[98:101], v[2:9], v[38:45], v[98:101], v170, v170 op_sel_hi:[0,0,0]
	v_mfma_scale_f32_16x16x128_f8f6f4 v[90:93], v[22:29], v[38:45], v[154:157], v170, v170 op_sel_hi:[0,0,0]
	v_mfma_scale_f32_16x16x128_f8f6f4 v[82:85], v[2:9], v[46:53], v[166:169], v170, v170 op_sel_hi:[0,0,0]
	v_mfma_scale_f32_16x16x128_f8f6f4 v[74:77], v[22:29], v[46:53], v[188:191], v170, v170 op_sel_hi:[0,0,0]
	s_setprio 0
	s_setprio 1
	v_mfma_scale_f32_16x16x128_f8f6f4 v[118:121], v[130:137], v[10:17], v[118:121], v170, v170 op_sel_hi:[0,0,0]
	v_mfma_scale_f32_16x16x128_f8f6f4 v[110:113], v[138:145], v[10:17], v[110:113], v170, v170 op_sel_hi:[0,0,0]
	v_mfma_scale_f32_16x16x128_f8f6f4 v[102:105], v[130:137], v[30:37], v[102:105], v170, v170 op_sel_hi:[0,0,0]
	v_mfma_scale_f32_16x16x128_f8f6f4 v[94:97], v[138:145], v[30:37], v[180:183], v170, v170 op_sel_hi:[0,0,0]
	v_mfma_scale_f32_16x16x128_f8f6f4 v[86:89], v[130:137], v[38:45], v[184:187], v170, v170 op_sel_hi:[0,0,0]
	v_mfma_scale_f32_16x16x128_f8f6f4 v[78:81], v[138:145], v[38:45], v[192:195], v170, v170 op_sel_hi:[0,0,0]
	v_mfma_scale_f32_16x16x128_f8f6f4 v[70:73], v[130:137], v[46:53], v[196:199], v170, v170 op_sel_hi:[0,0,0]
	v_mfma_scale_f32_16x16x128_f8f6f4 v[66:69], v[138:145], v[46:53], v[200:203], v170, v170 op_sel_hi:[0,0,0]
	s_setprio 0
	s_barrier
	s_add_i32 s2, s2, s37
	s_mov_b32 m0, s2
	v_lshl_add_u64 v[10:11], s[58:59], 0, v[164:165]
	v_lshl_add_u64 v[12:13], v[10:11], 0, s[22:23]
	global_load_lds_dwordx4 v[12:13], off
	v_lshl_add_u64 v[10:11], v[10:11], 0, s[24:25]
	s_add_i32 m0, s2, 0x2000
	s_add_i32 s2, s34, s37
	global_load_lds_dwordx4 v[10:11], off
	s_mov_b32 m0, s2
	v_lshl_add_u64 v[10:11], s[58:59], 0, v[164:165]
	v_lshl_add_u64 v[12:13], v[10:11], 0, s[26:27]
	global_load_lds_dwordx4 v[12:13], off
	v_lshl_add_u64 v[10:11], v[10:11], 0, s[28:29]
	s_add_i32 m0, s2, 0x2000
	s_nop 0
	global_load_lds_dwordx4 v[10:11], off
	s_mov_b32 m0, s64
	v_lshl_add_u64 v[10:11], s[56:57], 0, v[158:159]
	v_lshl_add_u64 v[12:13], v[10:11], 0, s[22:23]
	global_load_lds_dwordx4 v[12:13], off
	v_lshl_add_u64 v[10:11], v[10:11], 0, s[24:25]
	s_mov_b32 m0, s65
	s_nop 0
	global_load_lds_dwordx4 v[10:11], off
	v_add_u32_e32 v184, s67, v1
	ds_read_b128 v[42:45], v184 offset:49152
	ds_read_b128 v[46:49], v184 offset:50176
	ds_read_b128 v[146:149], v184 offset:51200
	ds_read_b128 v[150:153], v184 offset:52224
	ds_read_b128 v[172:175], v184 offset:53248
	ds_read_b128 v[176:179], v184 offset:54272
	ds_read_b128 v[180:183], v184 offset:55296
	ds_read_b128 v[184:187], v184 offset:56320
	s_waitcnt vmcnt(8)
	s_waitcnt lgkmcnt(0)
	s_barrier
	s_setprio 1
	s_waitcnt lgkmcnt(0)
	v_mfma_scale_f32_16x16x128_f8f6f4 v[54:57], v[2:9], v[42:49], v[54:57], v170, v170 op_sel_hi:[0,0,0]
	v_mfma_scale_f32_16x16x128_f8f6f4 v[50:53], v[22:29], v[42:49], v[204:207], v170, v170 op_sel_hi:[0,0,0]
	v_mfma_scale_f32_16x16x128_f8f6f4 v[38:41], v[2:9], v[146:153], v[208:211], v170, v170 op_sel_hi:[0,0,0]
	v_mfma_scale_f32_16x16x128_f8f6f4 v[30:33], v[22:29], v[146:153], v[212:215], v170, v170 op_sel_hi:[0,0,0]
	v_mfma_scale_f32_16x16x128_f8f6f4 v[18:21], v[2:9], v[172:179], v[18:21], v170, v170 op_sel_hi:[0,0,0]
	v_mfma_scale_f32_16x16x128_f8f6f4 v[10:13], v[22:29], v[172:179], v[216:219], v170, v170 op_sel_hi:[0,0,0]
	v_mfma_scale_f32_16x16x128_f8f6f4 v[6:9], v[2:9], v[180:187], v[220:223], v170, v170 op_sel_hi:[0,0,0]
	v_mfma_scale_f32_16x16x128_f8f6f4 v[2:5], v[22:29], v[180:187], v[224:227], v170, v170 op_sel_hi:[0,0,0]
	s_setprio 0
	s_setprio 1
	v_mfma_scale_f32_16x16x128_f8f6f4 v[62:65], v[130:137], v[42:49], v[62:65], v170, v170 op_sel_hi:[0,0,0]
	v_mfma_scale_f32_16x16x128_f8f6f4 v[58:61], v[138:145], v[42:49], v[58:61], v170, v170 op_sel_hi:[0,0,0]
	v_mfma_scale_f32_16x16x128_f8f6f4 v[46:49], v[130:137], v[146:153], v[228:231], v170, v170 op_sel_hi:[0,0,0]
	v_mfma_scale_f32_16x16x128_f8f6f4 v[42:45], v[138:145], v[146:153], v[232:235], v170, v170 op_sel_hi:[0,0,0]
	v_mfma_scale_f32_16x16x128_f8f6f4 v[34:37], v[130:137], v[172:179], v[236:239], v170, v170 op_sel_hi:[0,0,0]
	v_mfma_scale_f32_16x16x128_f8f6f4 v[26:29], v[138:145], v[172:179], v[240:243], v170, v170 op_sel_hi:[0,0,0]
	v_mfma_scale_f32_16x16x128_f8f6f4 v[22:25], v[130:137], v[180:187], v[244:247], v170, v170 op_sel_hi:[0,0,0]
	v_mfma_scale_f32_16x16x128_f8f6f4 v[14:17], v[138:145], v[180:187], v[248:251], v170, v170 op_sel_hi:[0,0,0]
	s_setprio 0
	s_barrier
	s_add_i32 s76, s76, 2
	s_add_u32 s54, s54, 0x100
	s_addc_u32 s55, s55, 0
	s_add_u32 s74, s74, 0x100
	s_addc_u32 s75, s75, 0
	s_cmp_gt_u32 s76, 13
	s_cbranch_scc0 .LBB0_1074
	s_and_b64 vcc, exec, s[30:31]
	s_cbranch_vccz .LBB0_1077
	s_barrier

.LBB0_1224:
	s_add_u32 s64, s46, s58
	v_add_u32_e32 v42, s76, v1
	v_add_u32_e32 v152, s79, v42
	v_add_u32_e32 v168, s81, v42
	s_addc_u32 s65, s47, s59
	s_add_u32 s34, s64, 0x100
	s_addc_u32 s35, s65, 0
	s_add_u32 s62, s2, s58
	s_addc_u32 s63, s49, s59
	s_cmpk_eq_i32 s58, 0x700
	s_cselect_b32 s61, s55, s35
	s_cselect_b32 s60, s54, s34
	s_cselect_b32 s63, s57, s63
	s_cselect_b32 s62, s56, s62
	s_add_i32 m0, s27, 0xc000
	v_lshl_add_u64 v[42:43], s[64:65], 0, v[130:131]
	v_lshl_add_u64 v[44:45], v[42:43], 0, s[38:39]
	global_load_lds_dwordx4 v[44:45], off
	v_lshl_add_u64 v[42:43], v[42:43], 0, s[40:41]
	s_add_i32 m0, s27, 0xe000
	s_nop 0
	global_load_lds_dwordx4 v[42:43], off
	ds_read_b128 v[140:143], v152
	ds_read_b128 v[144:147], v152 offset:1024
	ds_read_b128 v[148:151], v152 offset:2048
	ds_read_b128 v[152:155], v152 offset:3072
	ds_read_b128 v[156:159], v168
	ds_read_b128 v[160:163], v168 offset:1024
	ds_read_b128 v[164:167], v168 offset:2048
	ds_read_b128 v[168:171], v168 offset:3072
	v_add_u32_e32 v208, s77, v1
	v_mov_b64_e32 v[46:47], v[172:173]
	v_mov_b64_e32 v[50:51], v[176:177]
	v_mov_b64_e32 v[48:49], v[174:175]
	ds_read_b128 v[172:175], v208
	v_mov_b64_e32 v[52:53], v[178:179]
	ds_read_b128 v[176:179], v208 offset:1024
	ds_read_b128 v[180:183], v208 offset:2048
	ds_read_b128 v[184:187], v208 offset:3072
	ds_read_b128 v[196:199], v208 offset:4096
	ds_read_b128 v[200:203], v208 offset:5120
	ds_read_b128 v[204:207], v208 offset:6144
	ds_read_b128 v[208:211], v208 offset:7168
	s_waitcnt vmcnt(8)
	s_waitcnt lgkmcnt(0)
	s_barrier
	s_setprio 1
	s_waitcnt lgkmcnt(0)
	v_mfma_scale_f32_16x16x128_f8f6f4 v[94:97], v[140:147], v[172:179], v[94:97], v138, v138 op_sel_hi:[0,0,0]
	v_mfma_scale_f32_16x16x128_f8f6f4 v[90:93], v[148:155], v[172:179], v[90:93], v138, v138 op_sel_hi:[0,0,0]
	v_mfma_scale_f32_16x16x128_f8f6f4 v[86:89], v[140:147], v[180:187], v[86:89], v138, v138 op_sel_hi:[0,0,0]
	v_mfma_scale_f32_16x16x128_f8f6f4 v[82:85], v[148:155], v[180:187], v[82:85], v138, v138 op_sel_hi:[0,0,0]
	v_mfma_scale_f32_16x16x128_f8f6f4 v[78:81], v[140:147], v[196:203], v[78:81], v138, v138 op_sel_hi:[0,0,0]
	v_mfma_scale_f32_16x16x128_f8f6f4 v[74:77], v[148:155], v[196:203], v[74:77], v138, v138 op_sel_hi:[0,0,0]
	v_mfma_scale_f32_16x16x128_f8f6f4 v[134:137], v[140:147], v[204:211], v[70:73], v138, v138 op_sel_hi:[0,0,0]
	v_mfma_scale_f32_16x16x128_f8f6f4 v[188:191], v[148:155], v[204:211], v[66:69], v138, v138 op_sel_hi:[0,0,0]
	s_setprio 0
	s_setprio 1
	v_mfma_scale_f32_16x16x128_f8f6f4 v[192:195], v[156:163], v[172:179], v[62:65], v138, v138 op_sel_hi:[0,0,0]
	v_mfma_scale_f32_16x16x128_f8f6f4 v[172:175], v[164:171], v[172:179], v[58:61], v138, v138 op_sel_hi:[0,0,0]
	v_mfma_scale_f32_16x16x128_f8f6f4 v[176:179], v[156:163], v[180:187], v[54:57], v138, v138 op_sel_hi:[0,0,0]
	v_mfma_scale_f32_16x16x128_f8f6f4 v[180:183], v[164:171], v[180:187], v[50:53], v138, v138 op_sel_hi:[0,0,0]
	v_mfma_scale_f32_16x16x128_f8f6f4 v[184:187], v[156:163], v[196:203], v[46:49], v138, v138 op_sel_hi:[0,0,0]
	v_mfma_scale_f32_16x16x128_f8f6f4 v[196:199], v[164:171], v[196:203], v[18:21], v138, v138 op_sel_hi:[0,0,0]
	v_mfma_scale_f32_16x16x128_f8f6f4 v[200:203], v[156:163], v[204:211], v[6:9], v138, v138 op_sel_hi:[0,0,0]
	v_mfma_scale_f32_16x16x128_f8f6f4 v[204:207], v[164:171], v[204:211], v[14:17], v138, v138 op_sel_hi:[0,0,0]
	s_setprio 0
	s_barrier
	v_mov_b32_e32 v133, v131
	s_nop 2
	s_add_i32 s34, s79, s3
	s_mov_b32 m0, s34
	v_lshl_add_u64 v[6:7], s[62:63], 0, v[132:133]
	global_load_lds_dwordx4 v132, s[62:63]
	v_lshl_add_u64 v[6:7], v[6:7], 0, s[20:21]
	s_add_i32 m0, s34, 0x2000
	s_add_i32 s34, s81, s3
	global_load_lds_dwordx4 v[6:7], off
	s_mov_b32 m0, s34
	v_lshl_add_u64 v[6:7], s[62:63], 0, v[132:133]
	v_lshl_add_u64 v[8:9], v[6:7], 0, s[22:23]
	global_load_lds_dwordx4 v[8:9], off
	v_lshl_add_u64 v[6:7], v[6:7], 0, s[24:25]
	s_add_i32 m0, s34, 0x2000
	s_nop 0
	global_load_lds_dwordx4 v[6:7], off
	s_mov_b32 m0, s27
	v_lshl_add_u64 v[6:7], s[60:61], 0, v[130:131]
	global_load_lds_dwordx4 v130, s[60:61]
	v_lshl_add_u64 v[6:7], v[6:7], 0, s[20:21]
	s_mov_b32 m0, s70
	s_nop 0
	global_load_lds_dwordx4 v[6:7], off
	v_add_u32_e32 v70, s77, v1
	ds_read_b128 v[42:45], v70 offset:16384
	ds_read_b128 v[46:49], v70 offset:17408
	ds_read_b128 v[50:53], v70 offset:18432
	ds_read_b128 v[54:57], v70 offset:19456
	ds_read_b128 v[58:61], v70 offset:20480
	ds_read_b128 v[62:65], v70 offset:21504
	ds_read_b128 v[66:69], v70 offset:22528
	ds_read_b128 v[70:73], v70 offset:23552
	s_waitcnt vmcnt(8)
	s_waitcnt lgkmcnt(0)
	s_barrier
	s_setprio 1
	s_waitcnt lgkmcnt(0)
	v_mfma_scale_f32_16x16x128_f8f6f4 v[38:41], v[140:147], v[42:49], v[38:41], v138, v138 op_sel_hi:[0,0,0]
	v_mfma_scale_f32_16x16x128_f8f6f4 v[34:37], v[148:155], v[42:49], v[34:37], v138, v138 op_sel_hi:[0,0,0]
	v_mfma_scale_f32_16x16x128_f8f6f4 v[220:223], v[148:155], v[58:65], v[220:223], v138, v138 op_sel_hi:[0,0,0]
	v_mfma_scale_f32_16x16x128_f8f6f4 v[208:211], v[140:147], v[50:57], v[30:33], v138, v138 op_sel_hi:[0,0,0]
	v_mfma_scale_f32_16x16x128_f8f6f4 v[212:215], v[148:155], v[50:57], v[26:29], v138, v138 op_sel_hi:[0,0,0]
	v_mfma_scale_f32_16x16x128_f8f6f4 v[216:219], v[140:147], v[58:65], v[22:25], v138, v138 op_sel_hi:[0,0,0]
	v_mfma_scale_f32_16x16x128_f8f6f4 v[224:227], v[140:147], v[66:73], v[2:5], v138, v138 op_sel_hi:[0,0,0]
	v_mfma_scale_f32_16x16x128_f8f6f4 v[228:231], v[148:155], v[66:73], v[10:13], v138, v138 op_sel_hi:[0,0,0]
	s_setprio 0
	s_setprio 1
	v_mfma_scale_f32_16x16x128_f8f6f4 v[232:235], v[156:163], v[42:49], v[98:101], v138, v138 op_sel_hi:[0,0,0]
	v_mfma_scale_f32_16x16x128_f8f6f4 v[236:239], v[164:171], v[42:49], v[102:105], v138, v138 op_sel_hi:[0,0,0]
	v_mfma_scale_f32_16x16x128_f8f6f4 v[240:243], v[156:163], v[50:57], v[106:109], v138, v138 op_sel_hi:[0,0,0]
	v_mfma_scale_f32_16x16x128_f8f6f4 v[244:247], v[164:171], v[50:57], v[110:113], v138, v138 op_sel_hi:[0,0,0]
	v_mfma_scale_f32_16x16x128_f8f6f4 v[248:251], v[156:163], v[58:65], v[114:117], v138, v138 op_sel_hi:[0,0,0]
	v_mfma_scale_f32_16x16x128_f8f6f4 v[42:45], v[164:171], v[58:65], v[118:121], v138, v138 op_sel_hi:[0,0,0]
	v_mfma_scale_f32_16x16x128_f8f6f4 v[46:49], v[156:163], v[66:73], v[122:125], v138, v138 op_sel_hi:[0,0,0]
	v_mfma_scale_f32_16x16x128_f8f6f4 v[50:53], v[164:171], v[66:73], v[126:129], v138, v138 op_sel_hi:[0,0,0]
	s_setprio 0
	s_barrier
	s_mov_b32 m0, s71
	v_lshl_add_u64 v[54:55], s[60:61], 0, v[130:131]
	v_lshl_add_u64 v[56:57], v[54:55], 0, s[22:23]
	global_load_lds_dwordx4 v[56:57], off
	v_lshl_add_u64 v[54:55], v[54:55], 0, s[24:25]
	s_mov_b32 m0, s72
	s_nop 0
	global_load_lds_dwordx4 v[54:55], off
	s_add_i32 s34, 0, 0x18000
	v_add_u32_e32 v2, s76, v1
	s_add_i32 s35, 0, 0x1c000
	v_add_u32_e32 v110, s34, v2
	v_add_u32_e32 v144, s35, v2
	ds_read_b128 v[98:101], v110
	ds_read_b128 v[102:105], v110 offset:1024
	ds_read_b128 v[106:109], v110 offset:2048
	ds_read_b128 v[110:113], v110 offset:3072
	ds_read_b128 v[122:125], v144
	ds_read_b128 v[126:129], v144 offset:1024
	ds_read_b128 v[140:143], v144 offset:2048
	ds_read_b128 v[144:147], v144 offset:3072
	v_add_u32_e32 v30, s77, v1
	ds_read_b128 v[2:5], v30 offset:32768
	ds_read_b128 v[6:9], v30 offset:33792
	ds_read_b128 v[10:13], v30 offset:34816
	ds_read_b128 v[14:17], v30 offset:35840
	ds_read_b128 v[18:21], v30 offset:36864
	ds_read_b128 v[22:25], v30 offset:37888
	ds_read_b128 v[26:29], v30 offset:38912
	ds_read_b128 v[30:33], v30 offset:39936
	s_waitcnt vmcnt(8)
	s_waitcnt lgkmcnt(0)
	s_barrier
	s_setprio 1
	s_waitcnt lgkmcnt(0)
	v_mfma_scale_f32_16x16x128_f8f6f4 v[94:97], v[98:105], v[2:9], v[94:97], v138, v138 op_sel_hi:[0,0,0]
	v_mfma_scale_f32_16x16x128_f8f6f4 v[90:93], v[106:113], v[2:9], v[90:93], v138, v138 op_sel_hi:[0,0,0]
	v_mfma_scale_f32_16x16x128_f8f6f4 v[86:89], v[98:105], v[10:17], v[86:89], v138, v138 op_sel_hi:[0,0,0]
	v_mfma_scale_f32_16x16x128_f8f6f4 v[82:85], v[106:113], v[10:17], v[82:85], v138, v138 op_sel_hi:[0,0,0]
	v_mfma_scale_f32_16x16x128_f8f6f4 v[78:81], v[98:105], v[18:25], v[78:81], v138, v138 op_sel_hi:[0,0,0]
	v_mfma_scale_f32_16x16x128_f8f6f4 v[74:77], v[106:113], v[18:25], v[74:77], v138, v138 op_sel_hi:[0,0,0]
	v_mfma_scale_f32_16x16x128_f8f6f4 v[70:73], v[98:105], v[26:33], v[134:137], v138, v138 op_sel_hi:[0,0,0]
	v_mfma_scale_f32_16x16x128_f8f6f4 v[66:69], v[106:113], v[26:33], v[188:191], v138, v138 op_sel_hi:[0,0,0]
	s_setprio 0
	s_setprio 1
	v_mfma_scale_f32_16x16x128_f8f6f4 v[62:65], v[122:129], v[2:9], v[192:195], v138, v138 op_sel_hi:[0,0,0]
	v_mfma_scale_f32_16x16x128_f8f6f4 v[58:61], v[140:147], v[2:9], v[172:175], v138, v138 op_sel_hi:[0,0,0]
	v_mfma_scale_f32_16x16x128_f8f6f4 v[54:57], v[122:129], v[10:17], v[176:179], v138, v138 op_sel_hi:[0,0,0]
	v_mfma_scale_f32_16x16x128_f8f6f4 v[176:179], v[140:147], v[10:17], v[180:183], v138, v138 op_sel_hi:[0,0,0]
	v_mfma_scale_f32_16x16x128_f8f6f4 v[172:175], v[122:129], v[18:25], v[184:187], v138, v138 op_sel_hi:[0,0,0]
	v_mfma_scale_f32_16x16x128_f8f6f4 v[18:21], v[140:147], v[18:25], v[196:199], v138, v138 op_sel_hi:[0,0,0]
	v_mfma_scale_f32_16x16x128_f8f6f4 v[6:9], v[122:129], v[26:33], v[200:203], v138, v138 op_sel_hi:[0,0,0]
	v_mfma_scale_f32_16x16x128_f8f6f4 v[14:17], v[140:147], v[26:33], v[204:207], v138, v138 op_sel_hi:[0,0,0]
	s_setprio 0
	s_barrier
	s_add_i32 s34, s34, s3
	s_mov_b32 m0, s34
	v_lshl_add_u64 v[2:3], s[62:63], 0, v[132:133]
	v_lshl_add_u64 v[4:5], v[2:3], 0, s[30:31]
	global_load_lds_dwordx4 v[4:5], off
	v_lshl_add_u64 v[2:3], v[2:3], 0, s[36:37]
	s_add_i32 m0, s34, 0x2000
	s_add_i32 s34, s35, s3
	global_load_lds_dwordx4 v[2:3], off
	s_mov_b32 m0, s34
	v_lshl_add_u64 v[2:3], s[62:63], 0, v[132:133]
	v_lshl_add_u64 v[4:5], v[2:3], 0, s[38:39]
	global_load_lds_dwordx4 v[4:5], off
	v_lshl_add_u64 v[2:3], v[2:3], 0, s[40:41]
	s_add_i32 m0, s34, 0x2000
	s_nop 0
	global_load_lds_dwordx4 v[2:3], off
	s_mov_b32 m0, s73
	v_lshl_add_u64 v[2:3], s[60:61], 0, v[130:131]
	v_lshl_add_u64 v[4:5], v[2:3], 0, s[30:31]
	global_load_lds_dwordx4 v[4:5], off
	v_lshl_add_u64 v[2:3], v[2:3], 0, s[36:37]
	s_mov_b32 m0, s74
	s_nop 0
	global_load_lds_dwordx4 v[2:3], off
	v_add_u32_e32 v168, s77, v1
	ds_read_b128 v[114:117], v168 offset:49152
	ds_read_b128 v[118:121], v168 offset:50176
	ds_read_b128 v[148:151], v168 offset:51200
	ds_read_b128 v[152:155], v168 offset:52224
	ds_read_b128 v[156:159], v168 offset:53248
	ds_read_b128 v[160:163], v168 offset:54272
	ds_read_b128 v[164:167], v168 offset:55296
	ds_read_b128 v[168:171], v168 offset:56320
	s_waitcnt vmcnt(8)
	s_waitcnt lgkmcnt(0)
	s_barrier
	s_setprio 1
	s_waitcnt lgkmcnt(0)
	v_mfma_scale_f32_16x16x128_f8f6f4 v[38:41], v[98:105], v[114:121], v[38:41], v138, v138 op_sel_hi:[0,0,0]
	v_mfma_scale_f32_16x16x128_f8f6f4 v[34:37], v[106:113], v[114:121], v[34:37], v138, v138 op_sel_hi:[0,0,0]
	v_mfma_scale_f32_16x16x128_f8f6f4 v[30:33], v[98:105], v[148:155], v[208:211], v138, v138 op_sel_hi:[0,0,0]
	v_mfma_scale_f32_16x16x128_f8f6f4 v[26:29], v[106:113], v[148:155], v[212:215], v138, v138 op_sel_hi:[0,0,0]
	v_mfma_scale_f32_16x16x128_f8f6f4 v[22:25], v[98:105], v[156:163], v[216:219], v138, v138 op_sel_hi:[0,0,0]
	v_mfma_scale_f32_16x16x128_f8f6f4 v[220:223], v[106:113], v[156:163], v[220:223], v138, v138 op_sel_hi:[0,0,0]
	v_mfma_scale_f32_16x16x128_f8f6f4 v[2:5], v[98:105], v[164:171], v[224:227], v138, v138 op_sel_hi:[0,0,0]
	v_mfma_scale_f32_16x16x128_f8f6f4 v[10:13], v[106:113], v[164:171], v[228:231], v138, v138 op_sel_hi:[0,0,0]
	s_setprio 0
	s_setprio 1
	v_mfma_scale_f32_16x16x128_f8f6f4 v[98:101], v[122:129], v[114:121], v[232:235], v138, v138 op_sel_hi:[0,0,0]
	v_mfma_scale_f32_16x16x128_f8f6f4 v[102:105], v[140:147], v[114:121], v[236:239], v138, v138 op_sel_hi:[0,0,0]
	v_mfma_scale_f32_16x16x128_f8f6f4 v[106:109], v[122:129], v[148:155], v[240:243], v138, v138 op_sel_hi:[0,0,0]
	v_mfma_scale_f32_16x16x128_f8f6f4 v[110:113], v[140:147], v[148:155], v[244:247], v138, v138 op_sel_hi:[0,0,0]
	v_mfma_scale_f32_16x16x128_f8f6f4 v[114:117], v[122:129], v[156:163], v[248:251], v138, v138 op_sel_hi:[0,0,0]
	v_mfma_scale_f32_16x16x128_f8f6f4 v[118:121], v[140:147], v[156:163], v[42:45], v138, v138 op_sel_hi:[0,0,0]
	v_mfma_scale_f32_16x16x128_f8f6f4 v[122:125], v[122:129], v[164:171], v[46:49], v138, v138 op_sel_hi:[0,0,0]
	v_mfma_scale_f32_16x16x128_f8f6f4 v[126:129], v[140:147], v[164:171], v[50:53], v138, v138 op_sel_hi:[0,0,0]
	s_setprio 0
	s_barrier
	s_add_i32 s51, s51, 2
	s_add_u32 s58, s58, 0x100
	s_addc_u32 s59, s59, 0
	s_cmp_gt_u32 s51, 13
	s_cbranch_scc0 .LBB0_1224
	s_and_b64 vcc, exec, s[44:45]
	s_cbranch_vccz .LBB0_1227
	s_barrier

.LBB0_1257:
	s_add_u32 s60, s42, s54
	v_add_u32_e32 v42, s75, v1
	v_add_u32_e32 v152, s78, v42
	v_add_u32_e32 v168, s79, v42
	s_addc_u32 s61, s43, s55
	s_add_u32 s34, s60, 0x100
	s_addc_u32 s35, s61, 0
	s_add_u32 s58, s45, s54
	s_addc_u32 s59, s47, s55
	s_cmpk_eq_i32 s54, 0x700
	s_cselect_b32 s57, s51, s35
	s_cselect_b32 s56, s50, s34
	s_cselect_b32 s59, s53, s59
	s_cselect_b32 s58, s52, s58
	s_add_i32 m0, s23, 0xc000
	v_lshl_add_u64 v[42:43], s[60:61], 0, v[130:131]
	v_lshl_add_u64 v[44:45], v[42:43], 0, s[30:31]
	global_load_lds_dwordx4 v[44:45], off
	v_lshl_add_u64 v[42:43], v[42:43], 0, s[36:37]
	s_add_i32 m0, s23, 0xe000
	s_nop 0
	global_load_lds_dwordx4 v[42:43], off
	ds_read_b128 v[140:143], v152
	ds_read_b128 v[144:147], v152 offset:1024
	ds_read_b128 v[148:151], v152 offset:2048
	ds_read_b128 v[152:155], v152 offset:3072
	ds_read_b128 v[156:159], v168
	ds_read_b128 v[160:163], v168 offset:1024
	ds_read_b128 v[164:167], v168 offset:2048
	ds_read_b128 v[168:171], v168 offset:3072
	v_add_u32_e32 v208, s76, v1
	v_mov_b64_e32 v[46:47], v[172:173]
	v_mov_b64_e32 v[50:51], v[176:177]
	v_mov_b64_e32 v[48:49], v[174:175]
	ds_read_b128 v[172:175], v208
	v_mov_b64_e32 v[52:53], v[178:179]
	ds_read_b128 v[176:179], v208 offset:1024
	ds_read_b128 v[180:183], v208 offset:2048
	ds_read_b128 v[184:187], v208 offset:3072
	ds_read_b128 v[196:199], v208 offset:4096
	ds_read_b128 v[200:203], v208 offset:5120
	ds_read_b128 v[204:207], v208 offset:6144
	ds_read_b128 v[208:211], v208 offset:7168
	s_waitcnt vmcnt(8)
	s_waitcnt lgkmcnt(0)
	s_barrier
	s_setprio 1
	s_waitcnt lgkmcnt(0)
	v_mfma_scale_f32_16x16x128_f8f6f4 v[94:97], v[140:147], v[172:179], v[94:97], v138, v138 op_sel_hi:[0,0,0]
	v_mfma_scale_f32_16x16x128_f8f6f4 v[90:93], v[148:155], v[172:179], v[90:93], v138, v138 op_sel_hi:[0,0,0]
	v_mfma_scale_f32_16x16x128_f8f6f4 v[86:89], v[140:147], v[180:187], v[86:89], v138, v138 op_sel_hi:[0,0,0]
	v_mfma_scale_f32_16x16x128_f8f6f4 v[82:85], v[148:155], v[180:187], v[82:85], v138, v138 op_sel_hi:[0,0,0]
	v_mfma_scale_f32_16x16x128_f8f6f4 v[78:81], v[140:147], v[196:203], v[78:81], v138, v138 op_sel_hi:[0,0,0]
	v_mfma_scale_f32_16x16x128_f8f6f4 v[74:77], v[148:155], v[196:203], v[74:77], v138, v138 op_sel_hi:[0,0,0]
	v_mfma_scale_f32_16x16x128_f8f6f4 v[134:137], v[140:147], v[204:211], v[70:73], v138, v138 op_sel_hi:[0,0,0]
	v_mfma_scale_f32_16x16x128_f8f6f4 v[188:191], v[148:155], v[204:211], v[66:69], v138, v138 op_sel_hi:[0,0,0]
	s_setprio 0
	s_setprio 1
	v_mfma_scale_f32_16x16x128_f8f6f4 v[192:195], v[156:163], v[172:179], v[62:65], v138, v138 op_sel_hi:[0,0,0]
	v_mfma_scale_f32_16x16x128_f8f6f4 v[172:175], v[164:171], v[172:179], v[58:61], v138, v138 op_sel_hi:[0,0,0]
	v_mfma_scale_f32_16x16x128_f8f6f4 v[176:179], v[156:163], v[180:187], v[54:57], v138, v138 op_sel_hi:[0,0,0]
	v_mfma_scale_f32_16x16x128_f8f6f4 v[180:183], v[164:171], v[180:187], v[50:53], v138, v138 op_sel_hi:[0,0,0]
	v_mfma_scale_f32_16x16x128_f8f6f4 v[184:187], v[156:163], v[196:203], v[46:49], v138, v138 op_sel_hi:[0,0,0]
	v_mfma_scale_f32_16x16x128_f8f6f4 v[196:199], v[164:171], v[196:203], v[18:21], v138, v138 op_sel_hi:[0,0,0]
	v_mfma_scale_f32_16x16x128_f8f6f4 v[200:203], v[156:163], v[204:211], v[6:9], v138, v138 op_sel_hi:[0,0,0]
	v_mfma_scale_f32_16x16x128_f8f6f4 v[204:207], v[164:171], v[204:211], v[14:17], v138, v138 op_sel_hi:[0,0,0]
	s_setprio 0
	s_barrier
	v_mov_b32_e32 v133, v131
	s_nop 2
	s_add_i32 s34, s78, s39
	s_mov_b32 m0, s34
	v_lshl_add_u64 v[6:7], s[58:59], 0, v[132:133]
	global_load_lds_dwordx4 v132, s[58:59]
	v_lshl_add_u64 v[6:7], v[6:7], 0, s[8:9]
	s_add_i32 m0, s34, 0x2000
	s_add_i32 s34, s79, s39
	global_load_lds_dwordx4 v[6:7], off
	s_mov_b32 m0, s34
	v_lshl_add_u64 v[6:7], s[58:59], 0, v[132:133]
	v_lshl_add_u64 v[8:9], v[6:7], 0, s[18:19]
	global_load_lds_dwordx4 v[8:9], off
	v_lshl_add_u64 v[6:7], v[6:7], 0, s[20:21]
	s_add_i32 m0, s34, 0x2000
	s_nop 0
	global_load_lds_dwordx4 v[6:7], off
	s_mov_b32 m0, s23
	v_lshl_add_u64 v[6:7], s[56:57], 0, v[130:131]
	global_load_lds_dwordx4 v130, s[56:57]
	v_lshl_add_u64 v[6:7], v[6:7], 0, s[8:9]
	s_mov_b32 m0, s69
	s_nop 0
	global_load_lds_dwordx4 v[6:7], off
	v_add_u32_e32 v70, s76, v1
	ds_read_b128 v[42:45], v70 offset:16384
	ds_read_b128 v[46:49], v70 offset:17408
	ds_read_b128 v[50:53], v70 offset:18432
	ds_read_b128 v[54:57], v70 offset:19456
	ds_read_b128 v[58:61], v70 offset:20480
	ds_read_b128 v[62:65], v70 offset:21504
	ds_read_b128 v[66:69], v70 offset:22528
	ds_read_b128 v[70:73], v70 offset:23552
	s_waitcnt vmcnt(8)
	s_waitcnt lgkmcnt(0)
	s_barrier
	s_setprio 1
	s_waitcnt lgkmcnt(0)
	v_mfma_scale_f32_16x16x128_f8f6f4 v[38:41], v[140:147], v[42:49], v[38:41], v138, v138 op_sel_hi:[0,0,0]
	v_mfma_scale_f32_16x16x128_f8f6f4 v[34:37], v[148:155], v[42:49], v[34:37], v138, v138 op_sel_hi:[0,0,0]
	v_mfma_scale_f32_16x16x128_f8f6f4 v[220:223], v[148:155], v[58:65], v[220:223], v138, v138 op_sel_hi:[0,0,0]
	v_mfma_scale_f32_16x16x128_f8f6f4 v[208:211], v[140:147], v[50:57], v[30:33], v138, v138 op_sel_hi:[0,0,0]
	v_mfma_scale_f32_16x16x128_f8f6f4 v[212:215], v[148:155], v[50:57], v[26:29], v138, v138 op_sel_hi:[0,0,0]
	v_mfma_scale_f32_16x16x128_f8f6f4 v[216:219], v[140:147], v[58:65], v[22:25], v138, v138 op_sel_hi:[0,0,0]
	v_mfma_scale_f32_16x16x128_f8f6f4 v[224:227], v[140:147], v[66:73], v[2:5], v138, v138 op_sel_hi:[0,0,0]
	v_mfma_scale_f32_16x16x128_f8f6f4 v[228:231], v[148:155], v[66:73], v[10:13], v138, v138 op_sel_hi:[0,0,0]
	s_setprio 0
	s_setprio 1
	v_mfma_scale_f32_16x16x128_f8f6f4 v[232:235], v[156:163], v[42:49], v[98:101], v138, v138 op_sel_hi:[0,0,0]
	v_mfma_scale_f32_16x16x128_f8f6f4 v[236:239], v[164:171], v[42:49], v[102:105], v138, v138 op_sel_hi:[0,0,0]
	v_mfma_scale_f32_16x16x128_f8f6f4 v[240:243], v[156:163], v[50:57], v[106:109], v138, v138 op_sel_hi:[0,0,0]
	v_mfma_scale_f32_16x16x128_f8f6f4 v[244:247], v[164:171], v[50:57], v[110:113], v138, v138 op_sel_hi:[0,0,0]
	v_mfma_scale_f32_16x16x128_f8f6f4 v[248:251], v[156:163], v[58:65], v[114:117], v138, v138 op_sel_hi:[0,0,0]
	v_mfma_scale_f32_16x16x128_f8f6f4 v[42:45], v[164:171], v[58:65], v[118:121], v138, v138 op_sel_hi:[0,0,0]
	v_mfma_scale_f32_16x16x128_f8f6f4 v[46:49], v[156:163], v[66:73], v[122:125], v138, v138 op_sel_hi:[0,0,0]
	v_mfma_scale_f32_16x16x128_f8f6f4 v[50:53], v[164:171], v[66:73], v[126:129], v138, v138 op_sel_hi:[0,0,0]
	s_setprio 0
	s_barrier
	s_mov_b32 m0, s70
	v_lshl_add_u64 v[54:55], s[56:57], 0, v[130:131]
	v_lshl_add_u64 v[56:57], v[54:55], 0, s[18:19]
	global_load_lds_dwordx4 v[56:57], off
	v_lshl_add_u64 v[54:55], v[54:55], 0, s[20:21]
	s_mov_b32 m0, s71
	s_nop 0
	global_load_lds_dwordx4 v[54:55], off
	s_add_i32 s34, 0, 0x18000
	v_add_u32_e32 v2, s75, v1
	s_add_i32 s35, 0, 0x1c000
	v_add_u32_e32 v110, s34, v2
	v_add_u32_e32 v144, s35, v2
	ds_read_b128 v[98:101], v110
	ds_read_b128 v[102:105], v110 offset:1024
	ds_read_b128 v[106:109], v110 offset:2048
	ds_read_b128 v[110:113], v110 offset:3072
	ds_read_b128 v[122:125], v144
	ds_read_b128 v[126:129], v144 offset:1024
	ds_read_b128 v[140:143], v144 offset:2048
	ds_read_b128 v[144:147], v144 offset:3072
	v_add_u32_e32 v30, s76, v1
	ds_read_b128 v[2:5], v30 offset:32768
	ds_read_b128 v[6:9], v30 offset:33792
	ds_read_b128 v[10:13], v30 offset:34816
	ds_read_b128 v[14:17], v30 offset:35840
	ds_read_b128 v[18:21], v30 offset:36864
	ds_read_b128 v[22:25], v30 offset:37888
	ds_read_b128 v[26:29], v30 offset:38912
	ds_read_b128 v[30:33], v30 offset:39936
	s_waitcnt vmcnt(8)
	s_waitcnt lgkmcnt(0)
	s_barrier
	s_setprio 1
	s_waitcnt lgkmcnt(0)
	v_mfma_scale_f32_16x16x128_f8f6f4 v[94:97], v[98:105], v[2:9], v[94:97], v138, v138 op_sel_hi:[0,0,0]
	v_mfma_scale_f32_16x16x128_f8f6f4 v[90:93], v[106:113], v[2:9], v[90:93], v138, v138 op_sel_hi:[0,0,0]
	v_mfma_scale_f32_16x16x128_f8f6f4 v[86:89], v[98:105], v[10:17], v[86:89], v138, v138 op_sel_hi:[0,0,0]
	v_mfma_scale_f32_16x16x128_f8f6f4 v[82:85], v[106:113], v[10:17], v[82:85], v138, v138 op_sel_hi:[0,0,0]
	v_mfma_scale_f32_16x16x128_f8f6f4 v[78:81], v[98:105], v[18:25], v[78:81], v138, v138 op_sel_hi:[0,0,0]
	v_mfma_scale_f32_16x16x128_f8f6f4 v[74:77], v[106:113], v[18:25], v[74:77], v138, v138 op_sel_hi:[0,0,0]
	v_mfma_scale_f32_16x16x128_f8f6f4 v[70:73], v[98:105], v[26:33], v[134:137], v138, v138 op_sel_hi:[0,0,0]
	v_mfma_scale_f32_16x16x128_f8f6f4 v[66:69], v[106:113], v[26:33], v[188:191], v138, v138 op_sel_hi:[0,0,0]
	s_setprio 0
	s_setprio 1
	v_mfma_scale_f32_16x16x128_f8f6f4 v[62:65], v[122:129], v[2:9], v[192:195], v138, v138 op_sel_hi:[0,0,0]
	v_mfma_scale_f32_16x16x128_f8f6f4 v[58:61], v[140:147], v[2:9], v[172:175], v138, v138 op_sel_hi:[0,0,0]
	v_mfma_scale_f32_16x16x128_f8f6f4 v[54:57], v[122:129], v[10:17], v[176:179], v138, v138 op_sel_hi:[0,0,0]
	v_mfma_scale_f32_16x16x128_f8f6f4 v[176:179], v[140:147], v[10:17], v[180:183], v138, v138 op_sel_hi:[0,0,0]
	v_mfma_scale_f32_16x16x128_f8f6f4 v[172:175], v[122:129], v[18:25], v[184:187], v138, v138 op_sel_hi:[0,0,0]
	v_mfma_scale_f32_16x16x128_f8f6f4 v[18:21], v[140:147], v[18:25], v[196:199], v138, v138 op_sel_hi:[0,0,0]
	v_mfma_scale_f32_16x16x128_f8f6f4 v[6:9], v[122:129], v[26:33], v[200:203], v138, v138 op_sel_hi:[0,0,0]
	v_mfma_scale_f32_16x16x128_f8f6f4 v[14:17], v[140:147], v[26:33], v[204:207], v138, v138 op_sel_hi:[0,0,0]
	s_setprio 0
	s_barrier
	s_add_i32 s34, s34, s39
	s_mov_b32 m0, s34
	v_lshl_add_u64 v[2:3], s[58:59], 0, v[132:133]
	v_lshl_add_u64 v[4:5], v[2:3], 0, s[26:27]
	global_load_lds_dwordx4 v[4:5], off
	v_lshl_add_u64 v[2:3], v[2:3], 0, s[28:29]
	s_add_i32 m0, s34, 0x2000
	s_add_i32 s34, s35, s39
	global_load_lds_dwordx4 v[2:3], off
	s_mov_b32 m0, s34
	v_lshl_add_u64 v[2:3], s[58:59], 0, v[132:133]
	v_lshl_add_u64 v[4:5], v[2:3], 0, s[30:31]
	global_load_lds_dwordx4 v[4:5], off
	v_lshl_add_u64 v[2:3], v[2:3], 0, s[36:37]
	s_add_i32 m0, s34, 0x2000
	s_nop 0
	global_load_lds_dwordx4 v[2:3], off
	s_mov_b32 m0, s72
	v_lshl_add_u64 v[2:3], s[56:57], 0, v[130:131]
	v_lshl_add_u64 v[4:5], v[2:3], 0, s[26:27]
	global_load_lds_dwordx4 v[4:5], off
	v_lshl_add_u64 v[2:3], v[2:3], 0, s[28:29]
	s_mov_b32 m0, s73
	s_nop 0
	global_load_lds_dwordx4 v[2:3], off
	v_add_u32_e32 v168, s76, v1
	ds_read_b128 v[114:117], v168 offset:49152
	ds_read_b128 v[118:121], v168 offset:50176
	ds_read_b128 v[148:151], v168 offset:51200
	ds_read_b128 v[152:155], v168 offset:52224
	ds_read_b128 v[156:159], v168 offset:53248
	ds_read_b128 v[160:163], v168 offset:54272
	ds_read_b128 v[164:167], v168 offset:55296
	ds_read_b128 v[168:171], v168 offset:56320
	s_waitcnt vmcnt(8)
	s_waitcnt lgkmcnt(0)
	s_barrier
	s_setprio 1
	s_waitcnt lgkmcnt(0)
	v_mfma_scale_f32_16x16x128_f8f6f4 v[38:41], v[98:105], v[114:121], v[38:41], v138, v138 op_sel_hi:[0,0,0]
	v_mfma_scale_f32_16x16x128_f8f6f4 v[34:37], v[106:113], v[114:121], v[34:37], v138, v138 op_sel_hi:[0,0,0]
	v_mfma_scale_f32_16x16x128_f8f6f4 v[30:33], v[98:105], v[148:155], v[208:211], v138, v138 op_sel_hi:[0,0,0]
	v_mfma_scale_f32_16x16x128_f8f6f4 v[26:29], v[106:113], v[148:155], v[212:215], v138, v138 op_sel_hi:[0,0,0]
	v_mfma_scale_f32_16x16x128_f8f6f4 v[22:25], v[98:105], v[156:163], v[216:219], v138, v138 op_sel_hi:[0,0,0]
	v_mfma_scale_f32_16x16x128_f8f6f4 v[220:223], v[106:113], v[156:163], v[220:223], v138, v138 op_sel_hi:[0,0,0]
	v_mfma_scale_f32_16x16x128_f8f6f4 v[2:5], v[98:105], v[164:171], v[224:227], v138, v138 op_sel_hi:[0,0,0]
	v_mfma_scale_f32_16x16x128_f8f6f4 v[10:13], v[106:113], v[164:171], v[228:231], v138, v138 op_sel_hi:[0,0,0]
	s_setprio 0
	s_setprio 1
	v_mfma_scale_f32_16x16x128_f8f6f4 v[98:101], v[122:129], v[114:121], v[232:235], v138, v138 op_sel_hi:[0,0,0]
	v_mfma_scale_f32_16x16x128_f8f6f4 v[102:105], v[140:147], v[114:121], v[236:239], v138, v138 op_sel_hi:[0,0,0]
	v_mfma_scale_f32_16x16x128_f8f6f4 v[106:109], v[122:129], v[148:155], v[240:243], v138, v138 op_sel_hi:[0,0,0]
	v_mfma_scale_f32_16x16x128_f8f6f4 v[110:113], v[140:147], v[148:155], v[244:247], v138, v138 op_sel_hi:[0,0,0]
	v_mfma_scale_f32_16x16x128_f8f6f4 v[114:117], v[122:129], v[156:163], v[248:251], v138, v138 op_sel_hi:[0,0,0]
	v_mfma_scale_f32_16x16x128_f8f6f4 v[118:121], v[140:147], v[156:163], v[42:45], v138, v138 op_sel_hi:[0,0,0]
	v_mfma_scale_f32_16x16x128_f8f6f4 v[122:125], v[122:129], v[164:171], v[46:49], v138, v138 op_sel_hi:[0,0,0]
	v_mfma_scale_f32_16x16x128_f8f6f4 v[126:129], v[140:147], v[164:171], v[50:53], v138, v138 op_sel_hi:[0,0,0]
	s_setprio 0
	s_barrier
	s_add_i32 s86, s86, 2
	s_add_u32 s54, s54, 0x100
	s_addc_u32 s55, s55, 0
	s_cmp_gt_u32 s86, 13
	s_cbranch_scc0 .LBB0_1257
	s_and_b64 vcc, exec, s[40:41]
	s_cbranch_vccz .LBB0_1260
	s_barrier

.LBB0_1308:
	s_add_u32 s34, s4, 0xfffa0080
	s_addc_u32 s35, s5, -1
	s_cmp_eq_u32 s83, 12
	s_cselect_b32 s53, s45, s35
	s_cselect_b32 s52, s44, s34
	s_cselect_b32 s55, s47, s43
	s_cselect_b32 s54, s46, s41
	s_mov_b32 s34, 0xfffe0000
	s_mov_b32 s35, -1
	v_lshl_add_u64 v[192:193], s[4:5], 0, v[130:131]
	v_lshl_add_u64 v[192:193], v[192:193], 0, s[34:35]
	s_add_i32 m0, s51, 0xc000
	s_nop 0
	global_load_lds_dwordx4 v[192:193], off
	s_add_i32 m0, s51, 0xe000
	s_nop 0
	global_load_lds_dwordx4 v130, s[4:5]
	v_add_u32_e32 v133, s71, v1
	v_add_u32_e32 v148, s74, v133
	v_add_u32_e32 v164, s75, v133
	ds_read_b128 v[136:139], v148
	ds_read_b128 v[140:143], v148 offset:1024
	ds_read_b128 v[144:147], v148 offset:2048
	ds_read_b128 v[148:151], v148 offset:3072
	ds_read_b128 v[152:155], v164
	ds_read_b128 v[156:159], v164 offset:1024
	ds_read_b128 v[160:163], v164 offset:2048
	ds_read_b128 v[164:167], v164 offset:3072
	v_add_u32_e32 v133, s72, v1
	ds_read_b128 v[168:171], v133
	ds_read_b128 v[172:175], v133 offset:1024
	ds_read_b128 v[176:179], v133 offset:2048
	ds_read_b128 v[180:183], v133 offset:3072
	ds_read_b128 v[184:187], v133 offset:4096
	ds_read_b128 v[188:191], v133 offset:5120
	ds_read_b128 v[196:199], v133 offset:6144
	ds_read_b128 v[200:203], v133 offset:7168
	s_waitcnt vmcnt(8)
	s_waitcnt lgkmcnt(0)
	s_barrier
	s_setprio 1
	s_waitcnt lgkmcnt(0)
	v_mfma_scale_f32_16x16x128_f8f6f4 v[126:129], v[136:143], v[168:175], v[126:129], v134, v134 op_sel_hi:[0,0,0]
	v_mfma_scale_f32_16x16x128_f8f6f4 v[122:125], v[144:151], v[168:175], v[122:125], v134, v134 op_sel_hi:[0,0,0]
	v_mfma_scale_f32_16x16x128_f8f6f4 v[110:113], v[136:143], v[176:183], v[110:113], v134, v134 op_sel_hi:[0,0,0]
	v_mfma_scale_f32_16x16x128_f8f6f4 v[106:109], v[144:151], v[176:183], v[106:109], v134, v134 op_sel_hi:[0,0,0]
	v_mfma_scale_f32_16x16x128_f8f6f4 v[192:195], v[136:143], v[184:191], v[94:97], v134, v134 op_sel_hi:[0,0,0]
	v_mfma_scale_f32_16x16x128_f8f6f4 v[204:207], v[144:151], v[184:191], v[90:93], v134, v134 op_sel_hi:[0,0,0]
	v_mfma_scale_f32_16x16x128_f8f6f4 v[208:211], v[136:143], v[196:203], v[78:81], v134, v134 op_sel_hi:[0,0,0]
	v_mfma_scale_f32_16x16x128_f8f6f4 v[212:215], v[144:151], v[196:203], v[74:77], v134, v134 op_sel_hi:[0,0,0]
	s_setprio 0
	s_setprio 1
	v_mfma_scale_f32_16x16x128_f8f6f4 v[118:121], v[152:159], v[168:175], v[118:121], v134, v134 op_sel_hi:[0,0,0]
	v_mfma_scale_f32_16x16x128_f8f6f4 v[114:117], v[160:167], v[168:175], v[114:117], v134, v134 op_sel_hi:[0,0,0]
	v_mfma_scale_f32_16x16x128_f8f6f4 v[102:105], v[152:159], v[176:183], v[102:105], v134, v134 op_sel_hi:[0,0,0]
	v_mfma_scale_f32_16x16x128_f8f6f4 v[98:101], v[160:167], v[176:183], v[98:101], v134, v134 op_sel_hi:[0,0,0]
	v_mfma_scale_f32_16x16x128_f8f6f4 v[168:171], v[152:159], v[184:191], v[86:89], v134, v134 op_sel_hi:[0,0,0]
	v_mfma_scale_f32_16x16x128_f8f6f4 v[172:175], v[160:167], v[184:191], v[82:85], v134, v134 op_sel_hi:[0,0,0]
	v_mfma_scale_f32_16x16x128_f8f6f4 v[176:179], v[152:159], v[196:203], v[66:69], v134, v134 op_sel_hi:[0,0,0]
	v_mfma_scale_f32_16x16x128_f8f6f4 v[180:183], v[160:167], v[196:203], v[70:73], v134, v134 op_sel_hi:[0,0,0]
	s_setprio 0
	s_barrier
	v_mov_b32_e32 v133, v131
	s_add_i32 s34, s74, s62
	s_mov_b32 m0, s34
	v_lshl_add_u64 v[184:185], s[54:55], 0, v[132:133]
	global_load_lds_dwordx4 v132, s[54:55]
	v_lshl_add_u64 v[184:185], v[184:185], 0, s[8:9]
	s_add_i32 m0, s34, 0x2000
	s_add_i32 s34, s75, s62
	global_load_lds_dwordx4 v[184:185], off
	s_mov_b32 m0, s34
	v_lshl_add_u64 v[184:185], s[54:55], 0, v[132:133]
	v_lshl_add_u64 v[186:187], v[184:185], 0, s[12:13]
	global_load_lds_dwordx4 v[186:187], off
	v_lshl_add_u64 v[184:185], v[184:185], 0, s[14:15]
	s_add_i32 m0, s34, 0x2000
	s_nop 0
	global_load_lds_dwordx4 v[184:185], off
	s_mov_b32 m0, s51
	v_lshl_add_u64 v[184:185], s[52:53], 0, v[130:131]
	global_load_lds_dwordx4 v130, s[52:53]
	v_lshl_add_u64 v[184:185], v[184:185], 0, s[8:9]
	s_mov_b32 m0, s64
	s_nop 0
	global_load_lds_dwordx4 v[184:185], off
	v_add_u32_e32 v94, s72, v1
	ds_read_b128 v[66:69], v94 offset:16384
	ds_read_b128 v[70:73], v94 offset:17408
	ds_read_b128 v[74:77], v94 offset:18432
	ds_read_b128 v[78:81], v94 offset:19456
	ds_read_b128 v[82:85], v94 offset:20480
	ds_read_b128 v[86:89], v94 offset:21504
	ds_read_b128 v[90:93], v94 offset:22528
	ds_read_b128 v[94:97], v94 offset:23552
	s_waitcnt vmcnt(8)
	s_waitcnt lgkmcnt(0)
	s_barrier
	s_setprio 1
	s_waitcnt lgkmcnt(0)
	v_mfma_scale_f32_16x16x128_f8f6f4 v[62:65], v[136:143], v[66:73], v[62:65], v134, v134 op_sel_hi:[0,0,0]
	v_mfma_scale_f32_16x16x128_f8f6f4 v[58:61], v[144:151], v[66:73], v[58:61], v134, v134 op_sel_hi:[0,0,0]
	v_mfma_scale_f32_16x16x128_f8f6f4 v[10:13], v[136:143], v[90:97], v[10:13], v134, v134 op_sel_hi:[0,0,0]
	v_mfma_scale_f32_16x16x128_f8f6f4 v[184:187], v[136:143], v[74:81], v[46:49], v134, v134 op_sel_hi:[0,0,0]
	v_mfma_scale_f32_16x16x128_f8f6f4 v[188:191], v[144:151], v[74:81], v[42:45], v134, v134 op_sel_hi:[0,0,0]
	v_mfma_scale_f32_16x16x128_f8f6f4 v[196:199], v[136:143], v[82:89], v[30:33], v134, v134 op_sel_hi:[0,0,0]
	v_mfma_scale_f32_16x16x128_f8f6f4 v[200:203], v[144:151], v[82:89], v[26:29], v134, v134 op_sel_hi:[0,0,0]
	v_mfma_scale_f32_16x16x128_f8f6f4 v[216:219], v[144:151], v[90:97], v[14:17], v134, v134 op_sel_hi:[0,0,0]
	s_setprio 0
	s_setprio 1
	v_mfma_scale_f32_16x16x128_f8f6f4 v[54:57], v[152:159], v[66:73], v[54:57], v134, v134 op_sel_hi:[0,0,0]
	v_mfma_scale_f32_16x16x128_f8f6f4 v[220:223], v[160:167], v[66:73], v[50:53], v134, v134 op_sel_hi:[0,0,0]
	v_mfma_scale_f32_16x16x128_f8f6f4 v[224:227], v[152:159], v[74:81], v[38:41], v134, v134 op_sel_hi:[0,0,0]
	v_mfma_scale_f32_16x16x128_f8f6f4 v[228:231], v[160:167], v[74:81], v[34:37], v134, v134 op_sel_hi:[0,0,0]
	v_mfma_scale_f32_16x16x128_f8f6f4 v[232:235], v[152:159], v[82:89], v[22:25], v134, v134 op_sel_hi:[0,0,0]
	v_mfma_scale_f32_16x16x128_f8f6f4 v[236:239], v[160:167], v[82:89], v[18:21], v134, v134 op_sel_hi:[0,0,0]
	v_mfma_scale_f32_16x16x128_f8f6f4 v[240:243], v[152:159], v[90:97], v[6:9], v134, v134 op_sel_hi:[0,0,0]
	v_mfma_scale_f32_16x16x128_f8f6f4 v[244:247], v[160:167], v[90:97], v[2:5], v134, v134 op_sel_hi:[0,0,0]
	s_setprio 0
	s_barrier
	s_mov_b32 m0, s65
	v_lshl_add_u64 v[66:67], s[52:53], 0, v[130:131]
	v_lshl_add_u64 v[68:69], v[66:67], 0, s[12:13]
	global_load_lds_dwordx4 v[68:69], off
	v_lshl_add_u64 v[66:67], v[66:67], 0, s[14:15]
	s_mov_b32 m0, s66
	s_nop 0
	global_load_lds_dwordx4 v[66:67], off
	s_add_i32 s34, 0, 0x18000
	v_add_u32_e32 v22, s71, v1
	s_add_i32 s35, 0, 0x1c000
	v_add_u32_e32 v18, s34, v22
	v_add_u32_e32 v148, s35, v22
	ds_read_b128 v[2:5], v18
	ds_read_b128 v[6:9], v18 offset:1024
	ds_read_b128 v[14:17], v18 offset:2048
	ds_read_b128 v[18:21], v18 offset:3072
	ds_read_b128 v[136:139], v148
	ds_read_b128 v[140:143], v148 offset:1024
	ds_read_b128 v[144:147], v148 offset:2048
	ds_read_b128 v[148:151], v148 offset:3072
	v_add_u32_e32 v50, s72, v1
	ds_read_b128 v[22:25], v50 offset:32768
	ds_read_b128 v[26:29], v50 offset:33792
	ds_read_b128 v[30:33], v50 offset:34816
	ds_read_b128 v[34:37], v50 offset:35840
	ds_read_b128 v[38:41], v50 offset:36864
	ds_read_b128 v[42:45], v50 offset:37888
	ds_read_b128 v[46:49], v50 offset:38912
	ds_read_b128 v[50:53], v50 offset:39936
	s_waitcnt vmcnt(8)
	s_waitcnt lgkmcnt(0)
	s_barrier
	s_setprio 1
	s_waitcnt lgkmcnt(0)
	v_mfma_scale_f32_16x16x128_f8f6f4 v[126:129], v[2:9], v[22:29], v[126:129], v134, v134 op_sel_hi:[0,0,0]
	v_mfma_scale_f32_16x16x128_f8f6f4 v[122:125], v[14:21], v[22:29], v[122:125], v134, v134 op_sel_hi:[0,0,0]
	v_mfma_scale_f32_16x16x128_f8f6f4 v[110:113], v[2:9], v[30:37], v[110:113], v134, v134 op_sel_hi:[0,0,0]
	v_mfma_scale_f32_16x16x128_f8f6f4 v[106:109], v[14:21], v[30:37], v[106:109], v134, v134 op_sel_hi:[0,0,0]
	v_mfma_scale_f32_16x16x128_f8f6f4 v[94:97], v[2:9], v[38:45], v[192:195], v134, v134 op_sel_hi:[0,0,0]
	v_mfma_scale_f32_16x16x128_f8f6f4 v[90:93], v[14:21], v[38:45], v[204:207], v134, v134 op_sel_hi:[0,0,0]
	v_mfma_scale_f32_16x16x128_f8f6f4 v[78:81], v[2:9], v[46:53], v[208:211], v134, v134 op_sel_hi:[0,0,0]
	v_mfma_scale_f32_16x16x128_f8f6f4 v[74:77], v[14:21], v[46:53], v[212:215], v134, v134 op_sel_hi:[0,0,0]
	s_setprio 0
	s_setprio 1
	v_mfma_scale_f32_16x16x128_f8f6f4 v[118:121], v[136:143], v[22:29], v[118:121], v134, v134 op_sel_hi:[0,0,0]
	v_mfma_scale_f32_16x16x128_f8f6f4 v[114:117], v[144:151], v[22:29], v[114:117], v134, v134 op_sel_hi:[0,0,0]
	v_mfma_scale_f32_16x16x128_f8f6f4 v[102:105], v[136:143], v[30:37], v[102:105], v134, v134 op_sel_hi:[0,0,0]
	v_mfma_scale_f32_16x16x128_f8f6f4 v[98:101], v[144:151], v[30:37], v[98:101], v134, v134 op_sel_hi:[0,0,0]
	v_mfma_scale_f32_16x16x128_f8f6f4 v[86:89], v[136:143], v[38:45], v[168:171], v134, v134 op_sel_hi:[0,0,0]
	v_mfma_scale_f32_16x16x128_f8f6f4 v[82:85], v[144:151], v[38:45], v[172:175], v134, v134 op_sel_hi:[0,0,0]
	v_mfma_scale_f32_16x16x128_f8f6f4 v[66:69], v[136:143], v[46:53], v[176:179], v134, v134 op_sel_hi:[0,0,0]
	v_mfma_scale_f32_16x16x128_f8f6f4 v[70:73], v[144:151], v[46:53], v[180:183], v134, v134 op_sel_hi:[0,0,0]
	s_setprio 0
	s_barrier
	s_add_i32 s34, s34, s62
	s_mov_b32 m0, s34
	v_lshl_add_u64 v[22:23], s[54:55], 0, v[132:133]
	v_lshl_add_u64 v[24:25], v[22:23], 0, s[20:21]
	global_load_lds_dwordx4 v[24:25], off
	v_lshl_add_u64 v[22:23], v[22:23], 0, s[22:23]
	s_add_i32 m0, s34, 0x2000
	s_add_i32 s34, s35, s62
	global_load_lds_dwordx4 v[22:23], off
	s_mov_b32 m0, s34
	v_lshl_add_u64 v[22:23], s[54:55], 0, v[132:133]
	v_lshl_add_u64 v[24:25], v[22:23], 0, s[24:25]
	global_load_lds_dwordx4 v[24:25], off
	v_lshl_add_u64 v[22:23], v[22:23], 0, s[26:27]
	s_add_i32 m0, s34, 0x2000
	s_nop 0
	global_load_lds_dwordx4 v[22:23], off
	s_mov_b32 m0, s69
	v_lshl_add_u64 v[22:23], s[52:53], 0, v[130:131]
	v_lshl_add_u64 v[24:25], v[22:23], 0, s[20:21]
	global_load_lds_dwordx4 v[24:25], off
	v_lshl_add_u64 v[22:23], v[22:23], 0, s[22:23]
	s_mov_b32 m0, s70
	s_nop 0
	global_load_lds_dwordx4 v[22:23], off
	v_add_u32_e32 v172, s72, v1
	ds_read_b128 v[34:37], v172 offset:49152
	ds_read_b128 v[38:41], v172 offset:50176
	ds_read_b128 v[152:155], v172 offset:51200
	ds_read_b128 v[156:159], v172 offset:52224
	ds_read_b128 v[160:163], v172 offset:53248
	ds_read_b128 v[164:167], v172 offset:54272
	ds_read_b128 v[168:171], v172 offset:55296
	ds_read_b128 v[172:175], v172 offset:56320
	s_waitcnt vmcnt(8)
	s_waitcnt lgkmcnt(0)
	s_barrier
	s_setprio 1
	s_waitcnt lgkmcnt(0)
	v_mfma_scale_f32_16x16x128_f8f6f4 v[62:65], v[2:9], v[34:41], v[62:65], v134, v134 op_sel_hi:[0,0,0]
	v_mfma_scale_f32_16x16x128_f8f6f4 v[58:61], v[14:21], v[34:41], v[58:61], v134, v134 op_sel_hi:[0,0,0]
	v_mfma_scale_f32_16x16x128_f8f6f4 v[46:49], v[2:9], v[152:159], v[184:187], v134, v134 op_sel_hi:[0,0,0]
	v_mfma_scale_f32_16x16x128_f8f6f4 v[42:45], v[14:21], v[152:159], v[188:191], v134, v134 op_sel_hi:[0,0,0]
	v_mfma_scale_f32_16x16x128_f8f6f4 v[30:33], v[2:9], v[160:167], v[196:199], v134, v134 op_sel_hi:[0,0,0]
	v_mfma_scale_f32_16x16x128_f8f6f4 v[26:29], v[14:21], v[160:167], v[200:203], v134, v134 op_sel_hi:[0,0,0]
	v_mfma_scale_f32_16x16x128_f8f6f4 v[10:13], v[2:9], v[168:175], v[10:13], v134, v134 op_sel_hi:[0,0,0]
	v_mfma_scale_f32_16x16x128_f8f6f4 v[14:17], v[14:21], v[168:175], v[216:219], v134, v134 op_sel_hi:[0,0,0]
	s_setprio 0
	s_setprio 1
	v_mfma_scale_f32_16x16x128_f8f6f4 v[54:57], v[136:143], v[34:41], v[54:57], v134, v134 op_sel_hi:[0,0,0]
	v_mfma_scale_f32_16x16x128_f8f6f4 v[50:53], v[144:151], v[34:41], v[220:223], v134, v134 op_sel_hi:[0,0,0]
	v_mfma_scale_f32_16x16x128_f8f6f4 v[38:41], v[136:143], v[152:159], v[224:227], v134, v134 op_sel_hi:[0,0,0]
	v_mfma_scale_f32_16x16x128_f8f6f4 v[34:37], v[144:151], v[152:159], v[228:231], v134, v134 op_sel_hi:[0,0,0]
	v_mfma_scale_f32_16x16x128_f8f6f4 v[22:25], v[136:143], v[160:167], v[232:235], v134, v134 op_sel_hi:[0,0,0]
	v_mfma_scale_f32_16x16x128_f8f6f4 v[18:21], v[144:151], v[160:167], v[236:239], v134, v134 op_sel_hi:[0,0,0]
	v_mfma_scale_f32_16x16x128_f8f6f4 v[6:9], v[136:143], v[168:175], v[240:243], v134, v134 op_sel_hi:[0,0,0]
	v_mfma_scale_f32_16x16x128_f8f6f4 v[2:5], v[144:151], v[168:175], v[244:247], v134, v134 op_sel_hi:[0,0,0]
	s_setprio 0
	s_barrier
	s_add_i32 s83, s83, 2
	s_add_u32 s4, s4, 0x100
	s_addc_u32 s5, s5, 0
	s_add_u32 s41, s41, 0x100
	s_addc_u32 s43, s43, 0
	s_cmp_gt_u32 s83, 13
	s_cbranch_scc0 .LBB0_1308
	s_and_b64 vcc, exec, s[28:29]
	s_cbranch_vccz .LBB0_1311
	s_barrier
